# speedup vs baseline: 1.0115x; 1.0022x over previous
_Z11attn_kernelPKDF16_S0_PDF16_:
	s_load_dwordx4 s[4:7], s[0:1], 0x0
	s_load_dwordx2 s[8:9], s[0:1], 0x10
	s_lshr_b32 s1, s2, 3
	s_lshr_b32 s10, s2, 7
	s_and_b32 s0, s2, 4
	s_and_b32 s1, s1, 8
	s_and_b32 s20, s2, 3
	s_lshl_b32 s30, s10, 4
	s_or_b32 s22, s1, s0
	s_or_b32 s0, s30, s20
	s_or_b32 s14, s0, s22
	s_or_b32 s0, s20, 16
	s_sub_i32 s0, s0, s30
	s_mov_b32 s15, 0
	s_or_b32 s0, s0, s22
	s_bfe_u32 s24, s2, 0x30003
	s_ashr_i32 s1, s0, 31
	s_lshl_b64 s[2:3], s[14:15], 18
	s_waitcnt lgkmcnt(0)
	s_add_u32 s2, s4, s2
	s_addc_u32 s3, s5, s3
	s_lshl_b64 s[0:1], s[0:1], 18
	s_add_u32 s11, s4, s0
	s_addc_u32 s12, s5, s1
	s_add_u32 s13, s6, s0
	v_readfirstlane_b32 s16, v0
	s_addc_u32 s18, s7, s1
	s_lshl_b32 s0, s24, 2
	s_lshr_b32 s1, s16, 7
	s_add_i32 s14, s1, s0
	s_lshr_b32 s23, s16, 6
	s_lshl_b64 s[0:1], s[14:15], 13
	s_add_u32 s0, s2, s0
	v_and_b32_e32 v189, 31, v0
	s_addc_u32 s1, s3, s1
	s_lshl_b32 s21, s23, 5
	v_and_or_b32 v1, s21, 32, v189
	v_lshlrev_b32_e32 v186, 4, v1
	v_mov_b32_e32 v187, 0
	s_lshl_b32 s14, s23, 9
	v_lshl_add_u64 v[2:3], s[0:1], 0, v[186:187]
	s_and_b32 s0, s16, 0x3fffffc0
	s_lshl_b64 s[16:17], s[14:15], 1
	v_and_b32_e32 v188, 63, v0
	s_add_u32 s2, s11, s16
	s_addc_u32 s3, s12, s17
	s_add_u32 s44, s2, 0x8000
	s_addc_u32 s45, s3, 0
	v_lshlrev_b32_e32 v186, 4, v188
	v_lshl_add_u64 v[44:45], s[2:3], 0, v[186:187]
	s_add_u32 s2, s13, s16
	s_addc_u32 s3, s18, s17
	s_add_u32 s46, s2, 0x6000
	s_addc_u32 s47, s3, 0
	s_lshl_b32 s25, s23, 10
	s_cmp_lg_u32 0, -1
	s_cselect_b32 s1, 0, 0
	v_bfe_u32 v46, v0, 5, 1
	s_add_i32 s25, s25, s1
	s_mov_b32 s1, m0
	s_mov_b32 m0, s25
	s_nop 0
	global_load_lds_dwordx4 v[44:45], off
	s_mov_b32 m0, s1
	v_lshl_add_u64 v[34:35], s[2:3], 0, v[186:187]
	s_add_i32 s26, s25, 0x6000
	v_lshlrev_b32_e32 v4, 10, v46
	s_mov_b32 s1, m0
	s_mov_b32 m0, s26
	s_nop 0
	global_load_lds_dwordx4 v[34:35], off
	s_mov_b32 m0, s1
	s_mov_b64 s[18:19], 0x2000
	v_mov_b32_e32 v5, v187
	v_lshl_add_u64 v[6:7], v[44:45], 0, s[18:19]
	s_add_i32 s1, s25, 0x2000
	s_mov_b32 s2, m0
	s_mov_b32 m0, s1
	s_nop 0
	global_load_lds_dwordx4 v[6:7], off
	s_mov_b32 m0, s2
	v_lshl_add_u64 v[2:3], v[2:3], 0, v[4:5]
	global_load_dwordx4 v[136:139], v[2:3], off
	global_load_dwordx4 v[128:131], v[2:3], off offset:2048
	s_movk_i32 s1, 0x1000
	v_add_co_u32_e32 v2, vcc, s1, v2
	v_lshlrev_b32_e32 v1, 4, v189
	s_nop 0
	v_addc_co_u32_e32 v3, vcc, 0, v3, vcc
	global_load_dwordx4 v[120:123], v[2:3], off
	global_load_dwordx4 v[112:115], v[2:3], off offset:2048
	v_add3_u32 v184, 0, v4, v1
	v_mov_b32_e32 v2, v187
	v_mov_b32_e32 v3, v187
	v_mov_b32_e32 v4, v187
	v_mov_b32_e32 v6, v187
	v_mov_b32_e32 v7, v187
	v_mov_b32_e32 v8, v187
	v_mov_b32_e32 v9, v187
	v_mov_b32_e32 v10, v187
	v_mov_b32_e32 v11, v187
	v_mov_b32_e32 v12, v187
	v_mov_b32_e32 v13, v187
	v_mov_b32_e32 v14, v187
	v_mov_b32_e32 v15, v187
	v_mov_b32_e32 v16, v187
	v_mov_b32_e32 v17, v187
	s_mov_b64 s[2:3], 0x4000
	v_lshl_add_u64 v[18:19], v[44:45], 0, s[2:3]
	s_add_i32 s1, s25, 0x4000
	s_mov_b32 s11, m0
	s_mov_b32 m0, s1
	s_nop 0
	global_load_lds_dwordx4 v[18:19], off
	s_mov_b32 m0, s11
	v_lshl_add_u64 v[18:19], v[34:35], 0, s[18:19]
	s_add_i32 s1, s25, 0x8000
	s_mov_b32 s11, m0
	s_mov_b32 m0, s1
	s_nop 0
	global_load_lds_dwordx4 v[18:19], off
	s_mov_b32 m0, s11
	s_waitcnt vmcnt(4) lgkmcnt(0)
	s_barrier
	ds_read_b128 v[36:39], v184
	ds_read_b128 v[40:43], v184 offset:512
	v_lshlrev_b32_e32 v190, 3, v0
	s_mov_b64 s[12:13], 0x6000
	s_or_b32 s14, s22, s20
	s_sub_i32 s14, s14, s30
	s_add_i32 s34, s14, 16
	s_lshl_b32 s0, s0, 2
	s_ashr_i32 s35, s34, 31
	s_lshl_b64 s[34:35], s[34:35], 18
	s_mov_b32 s27, -1
	s_waitcnt vmcnt(3) lgkmcnt(1)
	v_mfma_f32_32x32x16_f16 v[18:33], v[36:39], v[136:139], v[2:17]
	s_movk_i32 s28, 0x6000
	s_movk_i32 s31, 0x2000
	s_movk_i32 s29, 0x4000
	v_lshlrev_b32_e32 v191, 9, v46
	v_lshlrev_b32_e32 v182, 4, v46
	v_lshlrev_b32_e32 v180, 4, v188
	s_waitcnt lgkmcnt(0)
	v_mfma_f32_32x32x16_f16 v[2:17], v[40:43], v[136:139], v[2:17]
	ds_read_b128 v[36:39], v184 offset:2048
	ds_read_b128 v[40:43], v184 offset:2560
	s_waitcnt vmcnt(2) lgkmcnt(1)
	v_mfma_f32_32x32x16_f16 v[18:33], v[36:39], v[128:131], v[18:33]
	s_waitcnt lgkmcnt(0)
	v_mfma_f32_32x32x16_f16 v[2:17], v[40:43], v[128:131], v[2:17]
	ds_read_b128 v[36:39], v184 offset:4096
	ds_read_b128 v[40:43], v184 offset:4608
	s_waitcnt vmcnt(1) lgkmcnt(1)
	v_mfma_f32_32x32x16_f16 v[18:33], v[36:39], v[120:123], v[18:33]
	s_waitcnt lgkmcnt(0)
	v_mfma_f32_32x32x16_f16 v[2:17], v[40:43], v[120:123], v[2:17]
	ds_read_b128 v[36:39], v184 offset:6144
	ds_read_b128 v[40:43], v184 offset:6656
	s_waitcnt vmcnt(0) lgkmcnt(1)
	v_mfma_f32_32x32x16_f16 v[18:33], v[36:39], v[112:115], v[18:33]
	s_waitcnt lgkmcnt(0)
	v_mfma_f32_32x32x16_f16 v[2:17], v[40:43], v[112:115], v[2:17]
	s_nop 11
	v_max_f32_e32 v1, v19, v18
	v_max3_f32 v37, v20, v21, v3
	v_max3_f32 v1, v1, v2, v4
	v_max3_f32 v36, v37, v24, v25
	v_max3_f32 v1, v1, v5, v22
	v_max3_f32 v36, v36, v8, v9
	v_max3_f32 v1, v1, v23, v6
	v_max3_f32 v36, v36, v28, v29
	v_max3_f32 v1, v1, v7, v26
	v_max3_f32 v36, v36, v12, v13
	v_max3_f32 v1, v1, v27, v10
	v_max3_f32 v36, v36, v32, v33
	v_max3_f32 v1, v1, v11, v30
	v_max3_f32 v36, v36, v16, v17
	v_max3_f32 v1, v1, v31, v14
	v_max3_f32 v1, v1, v15, v36
	v_mov_b32_e32 v36, v1
	s_nop 1
	v_permlane32_swap_b32_e32 v1, v36
	v_max_f32_e32 v183, v36, v1
	v_lshlrev_b32_e32 v1, 1, v0
	v_sub_f32_e32 v36, v2, v183
	v_and_b32_e32 v1, 32, v1
	v_and_b32_e32 v2, 24, v190
	v_lshlrev_b32_e32 v0, 4, v0
	v_add3_u32 v1, 0, v1, v2
	v_and_b32_e32 v0, 0xc0, v0
	v_lshlrev_b32_e32 v2, 8, v46
	v_add3_u32 v181, v1, v2, v0
	v_xor_b32_e32 v0, 0x80000000, v183
	v_sub_f32_e32 v37, v3, v183
	v_sub_f32_e32 v38, v4, v183
	v_sub_f32_e32 v39, v5, v183
	v_sub_f32_e32 v40, v6, v183
	v_sub_f32_e32 v41, v7, v183
	v_sub_f32_e32 v42, v8, v183
	v_sub_f32_e32 v43, v9, v183
	v_sub_f32_e32 v47, v10, v183
	v_sub_f32_e32 v57, v11, v183
	v_sub_f32_e32 v58, v12, v183
	v_sub_f32_e32 v59, v13, v183
	v_sub_f32_e32 v60, v14, v183
	v_sub_f32_e32 v61, v15, v183
	v_mov_b32_e32 v1, v0
	v_mov_b32_e32 v2, v0
	v_mov_b32_e32 v3, v0
	v_mov_b32_e32 v4, v0
	v_mov_b32_e32 v5, v0
	v_mov_b32_e32 v6, v0
	v_mov_b32_e32 v7, v0
	v_mov_b32_e32 v8, v0
	v_mov_b32_e32 v9, v0
	v_mov_b32_e32 v10, v0
	v_mov_b32_e32 v11, v0
	v_mov_b32_e32 v12, v0
	v_mov_b32_e32 v13, v0
	v_mov_b32_e32 v14, v0
	v_mov_b32_e32 v15, v0
	s_waitcnt vmcnt(0) lgkmcnt(0)
	s_barrier
	v_sub_f32_e32 v62, v16, v183
	v_sub_f32_e32 v63, v17, v183
	v_lshl_add_u64 v[16:17], v[44:45], 0, s[12:13]
	s_mov_b32 s1, m0
	s_mov_b32 m0, s25
	s_nop 0
	global_load_lds_dwordx4 v[16:17], off
	s_mov_b32 m0, s1
	s_add_i32 s1, s25, 0xa000
	v_lshl_add_u64 v[16:17], v[34:35], 0, s[2:3]
	s_mov_b32 s11, m0
	s_mov_b32 m0, s1
	s_nop 0
	global_load_lds_dwordx4 v[16:17], off
	s_mov_b32 m0, s11
	ds_read_b128 v[172:175], v184 offset:8192
	ds_read_b128 v[168:171], v184 offset:8704
	ds_read_b128 v[164:167], v184 offset:10240
	ds_read_b128 v[160:163], v184 offset:10752
	ds_read_b128 v[156:159], v184 offset:12288
	ds_read_b128 v[152:155], v184 offset:12800
	ds_read_b128 v[148:151], v184 offset:14336
	ds_read_b128 v[144:147], v184 offset:14848
	s_add_i32 s11, s0, 0
	v_sub_f32_e32 v18, v18, v183
	v_sub_f32_e32 v19, v19, v183
	v_sub_f32_e32 v20, v20, v183
	v_sub_f32_e32 v21, v21, v183
	v_sub_f32_e32 v22, v22, v183
	v_sub_f32_e32 v23, v23, v183
	v_sub_f32_e32 v24, v24, v183
	v_sub_f32_e32 v25, v25, v183
	v_sub_f32_e32 v26, v26, v183
	v_sub_f32_e32 v27, v27, v183
	v_sub_f32_e32 v28, v28, v183
	v_sub_f32_e32 v29, v29, v183
	v_sub_f32_e32 v30, v30, v183
	v_sub_f32_e32 v31, v31, v183
	v_sub_f32_e32 v32, v32, v183
	v_sub_f32_e32 v33, v33, v183
	s_add_u32 s14, s16, s34
	v_exp_f32_e32 v64, v18
	v_exp_f32_e32 v65, v19
	v_exp_f32_e32 v48, v36
	v_exp_f32_e32 v49, v37
	v_exp_f32_e32 v66, v20
	v_exp_f32_e32 v50, v38
	v_exp_f32_e32 v67, v21
	v_exp_f32_e32 v51, v39
	v_exp_f32_e32 v68, v22
	v_exp_f32_e32 v52, v40
	v_exp_f32_e32 v69, v23
	v_exp_f32_e32 v53, v41
	v_exp_f32_e32 v70, v24
	v_exp_f32_e32 v54, v42
	v_exp_f32_e32 v71, v25
	v_exp_f32_e32 v55, v43
	v_exp_f32_e32 v72, v26
	v_exp_f32_e32 v56, v47
	v_exp_f32_e32 v73, v27
	v_exp_f32_e32 v57, v57
	v_exp_f32_e32 v74, v28
	v_exp_f32_e32 v58, v58
	v_exp_f32_e32 v75, v29
	v_exp_f32_e32 v59, v59
	v_exp_f32_e32 v76, v30
	v_exp_f32_e32 v60, v60
	v_exp_f32_e32 v77, v31
	v_exp_f32_e32 v61, v61
	v_exp_f32_e32 v78, v32
	v_exp_f32_e32 v62, v62
	v_exp_f32_e32 v79, v33
	v_exp_f32_e32 v63, v63
	s_addc_u32 s16, s17, s35
	s_waitcnt vmcnt(2) lgkmcnt(0)
	s_barrier
	v_or_b32_e32 v16, s14, v186
	v_mov_b32_e32 v17, s16
	v_lshl_add_u64 v[16:17], v[16:17], 0, s[18:19]
	v_cmp_gt_u32_e64 s[0:1], 32, v188
	s_mov_b32 s16, 0x41000000
	s_mov_b32 s36, 0x43800000
	s_mov_b64 s[4:5], 0x8000
	s_movk_i32 s14, 0x2000
	s_movk_i32 s19, 0x4000
	v_mov_b32_e32 v16, v187
	v_mov_b32_e32 v17, v187
	v_mov_b32_e32 v18, v187
	v_mov_b32_e32 v19, v187
	v_mov_b32_e32 v20, v187
	v_mov_b32_e32 v21, v187
	v_mov_b32_e32 v22, v187
	v_mov_b32_e32 v23, v187
	v_mov_b32_e32 v24, v187
	v_mov_b32_e32 v25, v187
	v_mov_b32_e32 v26, v187
	v_mov_b32_e32 v27, v187
	v_mov_b32_e32 v28, v187
	v_mov_b32_e32 v29, v187
	v_mov_b32_e32 v30, v187
	v_mov_b32_e32 v31, v187
	v_mov_b32_e32 v32, v187
	v_mov_b32_e32 v33, v187
	v_mov_b32_e32 v34, v187
	v_mov_b32_e32 v35, v187
	v_mov_b32_e32 v36, v187
	v_mov_b32_e32 v37, v187
	v_mov_b32_e32 v38, v187
	v_mov_b32_e32 v39, v187
	v_mov_b32_e32 v40, v187
	v_mov_b32_e32 v41, v187
	v_mov_b32_e32 v42, v187
	v_mov_b32_e32 v43, v187
	v_mov_b32_e32 v44, v187
	v_mov_b32_e32 v45, v187
	v_mov_b32_e32 v46, v187
	v_mov_b32_e32 v47, v187
	v_lshl_add_u32 v186, v189, 2, s11
.LBB2_1:
	s_mov_b32 s17, s31
	s_mov_b32 s18, s15
	v_add_u32_e32 v185, s18, v181
	ds_read_b64_tr_b16 v[176:177], v185 offset:24576
	ds_read_b64_tr_b16 v[178:179], v185 offset:25088
	s_waitcnt lgkmcnt(9)
	v_mfma_f32_32x32x16_f16 v[96:111], v[172:175], v[136:139], v[0:15]
	v_add_f32_e32 v80, v64, v65
	v_add_f32_e32 v80, v66, v80
	v_add_f32_e32 v80, v67, v80
	v_add_f32_e32 v80, v68, v80
	v_add_f32_e32 v80, v69, v80
	v_cvt_pk_f16_f32 v140, v64, v65
	v_cvt_pk_f16_f32 v141, v66, v67
	ds_read_b64_tr_b16 v[172:173], v185 offset:28672
	ds_read_b64_tr_b16 v[174:175], v185 offset:29184
	v_add_f32_e32 v64, v70, v80
	s_waitcnt lgkmcnt(10)
	v_mfma_f32_32x32x16_f16 v[80:95], v[168:171], v[136:139], v[0:15]
	v_add_f32_e32 v64, v71, v64
	v_add_f32_e32 v64, v72, v64
	v_add_f32_e32 v64, v73, v64
	v_cvt_pk_f16_f32 v142, v68, v69
	v_cvt_pk_f16_f32 v143, v70, v71
	ds_read_b64_tr_b16 v[68:69], v185 offset:25600
	ds_read_b64_tr_b16 v[70:71], v185 offset:26112
	s_waitcnt lgkmcnt(11)
	v_mfma_f32_32x32x16_f16 v[96:111], v[164:167], v[128:131], v[96:111]
	v_add_f32_e32 v64, v74, v64
	v_add_f32_e32 v64, v75, v64
	v_add_f32_e32 v64, v76, v64
	v_add_f32_e32 v116, v77, v64
	v_cvt_pk_f16_f32 v132, v72, v73
	v_cvt_pk_f16_f32 v133, v74, v75
	ds_read_b64_tr_b16 v[64:65], v185 offset:29696
	ds_read_b64_tr_b16 v[66:67], v185 offset:30208
	s_waitcnt lgkmcnt(12)
	v_mfma_f32_32x32x16_f16 v[80:95], v[160:163], v[128:131], v[80:95]
	v_add_f32_e32 v72, v78, v116
	v_add_f32_e32 v72, v79, v72
	v_add_f32_e32 v72, v48, v72
	v_add_f32_e32 v116, v49, v72
	v_cvt_pk_f16_f32 v134, v76, v77
	v_cvt_pk_f16_f32 v135, v78, v79
	ds_read_b64_tr_b16 v[72:73], v185 offset:26624
	ds_read_b64_tr_b16 v[74:75], v185 offset:27136
	s_waitcnt lgkmcnt(13)
	v_mfma_f32_32x32x16_f16 v[96:111], v[156:159], v[120:123], v[96:111]
	v_add_f32_e32 v76, v50, v116
	v_add_f32_e32 v76, v51, v76
	v_add_f32_e32 v76, v52, v76
	v_add_f32_e32 v76, v53, v76
	v_cvt_pk_f16_f32 v124, v48, v49
	v_cvt_pk_f16_f32 v125, v50, v51
	ds_read_b64_tr_b16 v[48:49], v185 offset:30720
	ds_read_b64_tr_b16 v[50:51], v185 offset:31232
	s_waitcnt lgkmcnt(14)
	v_mfma_f32_32x32x16_f16 v[80:95], v[152:155], v[120:123], v[80:95]
	v_add_f32_e32 v76, v54, v76
	v_add_f32_e32 v76, v55, v76
	v_add_f32_e32 v76, v56, v76
	v_add_f32_e32 v76, v57, v76
	v_cvt_pk_f16_f32 v126, v52, v53
	v_cvt_pk_f16_f32 v127, v54, v55
	ds_read_b64_tr_b16 v[52:53], v185 offset:27648
	ds_read_b64_tr_b16 v[54:55], v185 offset:28160
	s_waitcnt lgkmcnt(14)
	v_mfma_f32_32x32x16_f16 v[96:111], v[148:151], v[112:115], v[96:111]
	v_add_f32_e32 v76, v58, v76
	v_add_f32_e32 v76, v59, v76
	v_add_f32_e32 v76, v60, v76
	v_add_f32_e32 v76, v61, v76
	v_cvt_pk_f16_f32 v116, v56, v57
	v_cvt_pk_f16_f32 v117, v58, v59
	ds_read_b64_tr_b16 v[56:57], v185 offset:31744
	ds_read_b64_tr_b16 v[58:59], v185 offset:32256
	v_mfma_f32_32x32x16_f16 v[80:95], v[144:147], v[112:115], v[80:95]
	v_add_f32_e32 v76, v62, v76
	v_add_f32_e32 v76, v63, v76
	v_cvt_pk_f16_f32 v118, v60, v61
	v_cvt_pk_f16_f32 v119, v62, v63
	s_add_i32 m0, s14, s25
	v_cmp_lt_f32_e32 vcc, s36, v76
	global_load_lds_dwordx4 v180, s[44:45]
	s_add_i32 m0, s28, s26
	s_add_u32 s44, s44, 0x2000
	global_load_lds_dwordx4 v180, s[46:47]
	s_addc_u32 s45, s45, 0
	s_add_u32 s46, s46, 0x2000
	s_addc_u32 s47, s47, 0
	s_cbranch_vccnz .Lmy_rare_1

.LBB2_2:
	s_waitcnt lgkmcnt(14)
	v_mfma_f32_32x32x16_f16 v[16:31], v[140:143], v[176:179], v[16:31]
	v_exp_f32_e32 v96, v96
	v_exp_f32_e32 v97, v97
	v_exp_f32_e32 v98, v98
	v_exp_f32_e32 v99, v99
	s_waitcnt lgkmcnt(12)
	v_mfma_f32_32x32x16_f16 v[32:47], v[140:143], v[172:175], v[32:47]
	v_exp_f32_e32 v100, v100
	v_exp_f32_e32 v101, v101
	v_exp_f32_e32 v102, v102
	v_exp_f32_e32 v103, v103
	v_add_u32_e32 v76, s19, v184
	ds_read_b128 v[60:63], v76
	ds_read_b128 v[148:151], v76 offset:512
	s_waitcnt lgkmcnt(12)
	v_mfma_f32_32x32x16_f16 v[16:31], v[132:135], v[68:71], v[16:31]
	v_exp_f32_e32 v104, v104
	v_exp_f32_e32 v105, v105
	v_exp_f32_e32 v106, v106
	v_exp_f32_e32 v107, v107
	ds_read_b128 v[176:179], v76 offset:2048
	ds_read_b128 v[172:175], v76 offset:2560
	s_waitcnt lgkmcnt(12)
	v_mfma_f32_32x32x16_f16 v[32:47], v[132:135], v[64:67], v[32:47]
	v_exp_f32_e32 v108, v108
	v_exp_f32_e32 v109, v109
	v_exp_f32_e32 v110, v110
	v_exp_f32_e32 v111, v111
	ds_read_b128 v[168:171], v76 offset:4096
	ds_read_b128 v[164:167], v76 offset:4608
	s_waitcnt lgkmcnt(12)
	v_mfma_f32_32x32x16_f16 v[16:31], v[124:127], v[72:75], v[16:31]
	v_exp_f32_e32 v80, v80
	v_exp_f32_e32 v81, v81
	v_exp_f32_e32 v82, v82
	v_exp_f32_e32 v83, v83
	ds_read_b128 v[160:163], v76 offset:6144
	ds_read_b128 v[156:159], v76 offset:6656
	s_waitcnt lgkmcnt(12)
	v_mfma_f32_32x32x16_f16 v[32:47], v[124:127], v[48:51], v[32:47]
	v_exp_f32_e32 v84, v84
	v_exp_f32_e32 v85, v85
	v_exp_f32_e32 v86, v86
	v_exp_f32_e32 v87, v87
	s_waitcnt lgkmcnt(10)
	v_mfma_f32_32x32x16_f16 v[16:31], v[116:119], v[52:55], v[16:31]
	v_exp_f32_e32 v88, v88
	v_exp_f32_e32 v89, v89
	v_exp_f32_e32 v90, v90
	v_exp_f32_e32 v91, v91
	s_waitcnt lgkmcnt(8)
	v_mfma_f32_32x32x16_f16 v[32:47], v[116:119], v[56:59], v[32:47]
	v_exp_f32_e32 v92, v92
	v_exp_f32_e32 v93, v93
	v_exp_f32_e32 v94, v94
	v_exp_f32_e32 v95, v95
	s_waitcnt vmcnt(3) lgkmcnt(0)
	s_barrier
.LBB2_4:
	v_add_u32_e32 v185, s17, v181
	ds_read_b64_tr_b16 v[144:145], v185 offset:24576
	ds_read_b64_tr_b16 v[146:147], v185 offset:25088
	s_waitcnt lgkmcnt(9)
	v_mfma_f32_32x32x16_f16 v[64:79], v[60:63], v[136:139], v[0:15]
	v_add_f32_e32 v48, v96, v97
	v_add_f32_e32 v48, v98, v48
	v_add_f32_e32 v48, v99, v48
	v_add_f32_e32 v48, v100, v48
	v_add_f32_e32 v48, v101, v48
	v_cvt_pk_f16_f32 v140, v96, v97
	v_cvt_pk_f16_f32 v141, v98, v99
	ds_read_b64_tr_b16 v[152:153], v185 offset:28672
	ds_read_b64_tr_b16 v[154:155], v185 offset:29184
	v_add_f32_e32 v48, v102, v48
	v_add_f32_e32 v48, v103, v48
	v_add_f32_e32 v48, v104, v48
	v_add_f32_e32 v96, v105, v48
	s_waitcnt lgkmcnt(10)
	v_mfma_f32_32x32x16_f16 v[48:63], v[148:151], v[136:139], v[0:15]
	v_cvt_pk_f16_f32 v142, v100, v101
	v_cvt_pk_f16_f32 v143, v102, v103
	ds_read_b64_tr_b16 v[148:149], v185 offset:25600
	ds_read_b64_tr_b16 v[150:151], v185 offset:26112
	s_waitcnt lgkmcnt(11)
	v_mfma_f32_32x32x16_f16 v[64:79], v[176:179], v[128:131], v[64:79]
	v_add_f32_e32 v96, v106, v96
	v_add_f32_e32 v96, v107, v96
	v_add_f32_e32 v96, v108, v96
	v_add_f32_e32 v96, v109, v96
	v_cvt_pk_f16_f32 v132, v104, v105
	v_cvt_pk_f16_f32 v133, v106, v107
	ds_read_b64_tr_b16 v[100:101], v185 offset:29696
	ds_read_b64_tr_b16 v[102:103], v185 offset:30208
	s_waitcnt lgkmcnt(12)
	v_mfma_f32_32x32x16_f16 v[48:63], v[172:175], v[128:131], v[48:63]
	v_add_f32_e32 v96, v110, v96
	v_add_f32_e32 v96, v111, v96
	v_add_f32_e32 v96, v80, v96
	v_add_f32_e32 v104, v81, v96
	v_cvt_pk_f16_f32 v134, v108, v109
	v_cvt_pk_f16_f32 v135, v110, v111
	ds_read_b64_tr_b16 v[96:97], v185 offset:26624
	ds_read_b64_tr_b16 v[98:99], v185 offset:27136
	s_waitcnt lgkmcnt(13)
	v_mfma_f32_32x32x16_f16 v[64:79], v[168:171], v[120:123], v[64:79]
	v_add_f32_e32 v104, v82, v104
	v_add_f32_e32 v104, v83, v104
	v_add_f32_e32 v104, v84, v104
	v_add_f32_e32 v104, v85, v104
	v_cvt_pk_f16_f32 v124, v80, v81
	v_cvt_pk_f16_f32 v125, v82, v83
	ds_read_b64_tr_b16 v[80:81], v185 offset:30720
	ds_read_b64_tr_b16 v[82:83], v185 offset:31232
	s_waitcnt lgkmcnt(14)
	v_mfma_f32_32x32x16_f16 v[48:63], v[164:167], v[120:123], v[48:63]
	v_add_f32_e32 v104, v86, v104
	v_add_f32_e32 v104, v87, v104
	v_add_f32_e32 v104, v88, v104
	v_add_f32_e32 v104, v89, v104
	v_cvt_pk_f16_f32 v126, v84, v85
	v_cvt_pk_f16_f32 v127, v86, v87
	ds_read_b64_tr_b16 v[84:85], v185 offset:27648
	ds_read_b64_tr_b16 v[86:87], v185 offset:28160
	s_waitcnt lgkmcnt(14)
	v_mfma_f32_32x32x16_f16 v[64:79], v[160:163], v[112:115], v[64:79]
	v_add_f32_e32 v104, v90, v104
	v_add_f32_e32 v104, v91, v104
	v_add_f32_e32 v104, v92, v104
	v_add_f32_e32 v104, v93, v104
	v_cvt_pk_f16_f32 v116, v88, v89
	v_cvt_pk_f16_f32 v117, v90, v91
	ds_read_b64_tr_b16 v[88:89], v185 offset:31744
	ds_read_b64_tr_b16 v[90:91], v185 offset:32256
	v_mfma_f32_32x32x16_f16 v[48:63], v[156:159], v[112:115], v[48:63]
	v_add_f32_e32 v104, v94, v104
	v_add_f32_e32 v104, v95, v104
	v_cvt_pk_f16_f32 v118, v92, v93
	v_cvt_pk_f16_f32 v119, v94, v95
	s_add_i32 m0, s19, s25
	v_cmp_lt_f32_e32 vcc, s36, v104
	global_load_lds_dwordx4 v180, s[44:45]
	s_add_i32 m0, s18, s26
	s_add_u32 s44, s44, 0x2000
	global_load_lds_dwordx4 v180, s[46:47]
	s_addc_u32 s45, s45, 0
	s_add_u32 s46, s46, 0x2000
	s_addc_u32 s47, s47, 0
	s_cbranch_vccnz .Lmy_rare_2

.LBB2_5:
	s_add_i32 s14, s19, 0x2000
	s_cmpk_lg_i32 s19, 0x4000
	s_cselect_b32 s14, s14, 0
	s_waitcnt lgkmcnt(14)
	v_mfma_f32_32x32x16_f16 v[16:31], v[140:143], v[144:147], v[16:31]
	v_exp_f32_e32 v64, v64
	v_exp_f32_e32 v65, v65
	v_exp_f32_e32 v66, v66
	v_exp_f32_e32 v67, v67
	s_waitcnt lgkmcnt(12)
	v_mfma_f32_32x32x16_f16 v[32:47], v[140:143], v[152:155], v[32:47]
	v_exp_f32_e32 v68, v68
	v_exp_f32_e32 v69, v69
	v_exp_f32_e32 v70, v70
	v_exp_f32_e32 v71, v71
	v_add_u32_e32 v92, s14, v184
	ds_read_b128 v[172:175], v92
	ds_read_b128 v[168:171], v92 offset:512
	s_waitcnt lgkmcnt(12)
	v_mfma_f32_32x32x16_f16 v[16:31], v[132:135], v[148:151], v[16:31]
	v_exp_f32_e32 v72, v72
	v_exp_f32_e32 v73, v73
	v_exp_f32_e32 v74, v74
	v_exp_f32_e32 v75, v75
	ds_read_b128 v[164:167], v92 offset:2048
	ds_read_b128 v[160:163], v92 offset:2560
	s_waitcnt lgkmcnt(12)
	v_mfma_f32_32x32x16_f16 v[32:47], v[132:135], v[100:103], v[32:47]
	v_exp_f32_e32 v76, v76
	v_exp_f32_e32 v77, v77
	v_exp_f32_e32 v78, v78
	v_exp_f32_e32 v79, v79
	ds_read_b128 v[156:159], v92 offset:4096
	ds_read_b128 v[152:155], v92 offset:4608
	s_waitcnt lgkmcnt(12)
	v_mfma_f32_32x32x16_f16 v[16:31], v[124:127], v[96:99], v[16:31]
	v_exp_f32_e32 v48, v48
	v_exp_f32_e32 v49, v49
	v_exp_f32_e32 v50, v50
	v_exp_f32_e32 v51, v51
	ds_read_b128 v[148:151], v92 offset:6144
	ds_read_b128 v[144:147], v92 offset:6656
	s_waitcnt lgkmcnt(12)
	v_mfma_f32_32x32x16_f16 v[32:47], v[124:127], v[80:83], v[32:47]
	v_exp_f32_e32 v52, v52
	v_exp_f32_e32 v53, v53
	v_exp_f32_e32 v54, v54
	v_exp_f32_e32 v55, v55
	s_waitcnt lgkmcnt(10)
	v_mfma_f32_32x32x16_f16 v[16:31], v[116:119], v[84:87], v[16:31]
	v_exp_f32_e32 v56, v56
	v_exp_f32_e32 v57, v57
	v_exp_f32_e32 v58, v58
	v_exp_f32_e32 v59, v59
	s_waitcnt lgkmcnt(8)
	v_mfma_f32_32x32x16_f16 v[32:47], v[116:119], v[88:91], v[32:47]
	v_exp_f32_e32 v60, v60
	v_exp_f32_e32 v61, v61
	v_exp_f32_e32 v62, v62
	v_exp_f32_e32 v63, v63
	s_add_i32 s6, s14, 0x2000
	s_cmpk_lg_i32 s14, 0x4000
	s_cselect_b32 s19, s6, 0
	s_add_i32 s27, s27, 2
	s_mov_b32 s15, s29
	s_mov_b32 s31, s28
	s_mov_b32 s29, s18
	s_mov_b32 s28, s17
	s_cmp_gt_u32 s27, 28
	s_waitcnt vmcnt(3) lgkmcnt(0)
	s_barrier
	s_cbranch_scc0 .LBB2_1
.LBB2_15:
	ds_read_b64_tr_b16 v[96:97], v181 offset:40960
	ds_read_b64_tr_b16 v[98:99], v181 offset:41472
	v_add_f32_e32 v80, v64, v65
	v_add_f32_e32 v80, v66, v80
	v_add_f32_e32 v80, v67, v80
	v_add_f32_e32 v80, v68, v80
	v_add_f32_e32 v100, v69, v80
	s_waitcnt lgkmcnt(9)
	v_mfma_f32_32x32x16_f16 v[80:95], v[172:175], v[136:139], v[0:15]
	v_cvt_pk_f16_f32 v140, v64, v65
	v_cvt_pk_f16_f32 v141, v66, v67
	ds_read_b64_tr_b16 v[64:65], v181 offset:45056
	ds_read_b64_tr_b16 v[66:67], v181 offset:45568
	s_waitcnt lgkmcnt(10)
	v_mfma_f32_32x32x16_f16 v[0:15], v[168:171], v[136:139], v[0:15]
	v_add_f32_e32 v100, v70, v100
	v_add_f32_e32 v100, v71, v100
	v_add_f32_e32 v100, v72, v100
	v_add_f32_e32 v100, v73, v100
	v_cvt_pk_f16_f32 v142, v68, v69
	v_cvt_pk_f16_f32 v143, v70, v71
	ds_read_b64_tr_b16 v[68:69], v181 offset:41984
	ds_read_b64_tr_b16 v[70:71], v181 offset:42496
	s_waitcnt lgkmcnt(11)
	v_mfma_f32_32x32x16_f16 v[80:95], v[164:167], v[128:131], v[80:95]
	v_add_f32_e32 v100, v74, v100
	v_add_f32_e32 v100, v75, v100
	v_add_f32_e32 v100, v76, v100
	v_add_f32_e32 v100, v77, v100
	v_cvt_pk_f16_f32 v132, v72, v73
	v_cvt_pk_f16_f32 v133, v74, v75
	ds_read_b64_tr_b16 v[72:73], v181 offset:46080
	ds_read_b64_tr_b16 v[74:75], v181 offset:46592
	s_waitcnt lgkmcnt(12)
	v_mfma_f32_32x32x16_f16 v[0:15], v[160:163], v[128:131], v[0:15]
	v_add_f32_e32 v100, v78, v100
	v_add_f32_e32 v100, v79, v100
	v_add_f32_e32 v100, v48, v100
	v_add_f32_e32 v100, v49, v100
	v_cvt_pk_f16_f32 v134, v76, v77
	v_cvt_pk_f16_f32 v135, v78, v79
	ds_read_b64_tr_b16 v[76:77], v181 offset:43008
	ds_read_b64_tr_b16 v[78:79], v181 offset:43520
	s_waitcnt lgkmcnt(13)
	v_mfma_f32_32x32x16_f16 v[80:95], v[156:159], v[120:123], v[80:95]
	v_add_f32_e32 v100, v50, v100
	v_add_f32_e32 v100, v51, v100
	v_add_f32_e32 v100, v52, v100
	v_add_f32_e32 v104, v53, v100
	v_cvt_pk_f16_f32 v124, v48, v49
	v_cvt_pk_f16_f32 v125, v50, v51
	ds_read_b64_tr_b16 v[100:101], v181 offset:47104
	ds_read_b64_tr_b16 v[102:103], v181 offset:47616
	s_waitcnt lgkmcnt(14)
	v_mfma_f32_32x32x16_f16 v[0:15], v[152:155], v[120:123], v[0:15]
	v_add_f32_e32 v48, v54, v104
	v_add_f32_e32 v48, v55, v48
	v_add_f32_e32 v48, v56, v48
	v_add_f32_e32 v48, v57, v48
	v_cvt_pk_f16_f32 v126, v52, v53
	v_cvt_pk_f16_f32 v127, v54, v55
	ds_read_b64_tr_b16 v[104:105], v181 offset:44032
	ds_read_b64_tr_b16 v[106:107], v181 offset:44544
	s_waitcnt lgkmcnt(14)
	v_mfma_f32_32x32x16_f16 v[80:95], v[148:151], v[112:115], v[80:95]
	v_add_f32_e32 v48, v58, v48
	v_add_f32_e32 v48, v59, v48
	v_add_f32_e32 v48, v60, v48
	v_add_f32_e32 v48, v61, v48
	v_cvt_pk_f16_f32 v116, v56, v57
	v_cvt_pk_f16_f32 v117, v58, v59
	ds_read_b64_tr_b16 v[108:109], v181 offset:48128
	ds_read_b64_tr_b16 v[110:111], v181 offset:48640
	v_mfma_f32_32x32x16_f16 v[0:15], v[144:147], v[112:115], v[0:15]
	v_add_f32_e32 v48, v62, v48
	v_add_f32_e32 v48, v63, v48
	v_cvt_pk_f16_f32 v118, v60, v61
	v_cvt_pk_f16_f32 v119, v62, v63
	s_nop 0
	v_cmp_lt_f32_e32 vcc, s36, v48
	s_nop 4
	s_cbranch_vccnz .Lmy_rare_3
.Lmy_back_3:
	v_add_f32_e32 v176, v187, v48
	s_nop 7
	s_nop 3
.LBB2_16:
	s_waitcnt lgkmcnt(14)
	v_mfma_f32_32x32x16_f16 v[16:31], v[140:143], v[96:99], v[16:31]
	v_exp_f32_e32 v80, v80
	v_exp_f32_e32 v81, v81
	v_exp_f32_e32 v82, v82
	v_exp_f32_e32 v83, v83
	s_waitcnt lgkmcnt(12)
	v_mfma_f32_32x32x16_f16 v[32:47], v[140:143], v[64:67], v[32:47]
	v_exp_f32_e32 v84, v84
	v_exp_f32_e32 v85, v85
	v_exp_f32_e32 v86, v86
	v_exp_f32_e32 v87, v87
	s_waitcnt lgkmcnt(10)
	v_mfma_f32_32x32x16_f16 v[16:31], v[132:135], v[68:71], v[16:31]
	v_exp_f32_e32 v88, v88
	v_exp_f32_e32 v89, v89
	v_exp_f32_e32 v90, v90
	v_exp_f32_e32 v91, v91
	s_waitcnt lgkmcnt(8)
	v_mfma_f32_32x32x16_f16 v[32:47], v[132:135], v[72:75], v[32:47]
	v_exp_f32_e32 v92, v92
	v_exp_f32_e32 v93, v93
	v_exp_f32_e32 v94, v94
	v_exp_f32_e32 v95, v95
	s_waitcnt lgkmcnt(6)
	v_mfma_f32_32x32x16_f16 v[16:31], v[124:127], v[76:79], v[16:31]
	v_exp_f32_e32 v0, v0
	v_exp_f32_e32 v1, v1
	v_exp_f32_e32 v2, v2
	v_exp_f32_e32 v3, v3
	s_waitcnt lgkmcnt(4)
	v_mfma_f32_32x32x16_f16 v[32:47], v[124:127], v[100:103], v[32:47]
	v_exp_f32_e32 v4, v4
	v_exp_f32_e32 v5, v5
	v_exp_f32_e32 v6, v6
	v_exp_f32_e32 v7, v7
	s_waitcnt lgkmcnt(2)
	v_mfma_f32_32x32x16_f16 v[16:31], v[116:119], v[104:107], v[16:31]
	v_exp_f32_e32 v8, v8
	v_exp_f32_e32 v9, v9
	v_exp_f32_e32 v10, v10
	v_exp_f32_e32 v11, v11
	s_waitcnt lgkmcnt(0)
	v_mfma_f32_32x32x16_f16 v[32:47], v[116:119], v[108:111], v[32:47]
	v_exp_f32_e32 v12, v12
	v_exp_f32_e32 v13, v13
	v_exp_f32_e32 v14, v14
	v_exp_f32_e32 v15, v15
	v_add_u32_e32 v48, s11, v182
.LBB2_18:
	s_waitcnt vmcnt(0) lgkmcnt(0)
	s_barrier
	v_add_f32_e32 v177, v80, v81
	v_add_f32_e32 v177, v82, v177
	v_add_f32_e32 v177, v83, v177
	v_add_f32_e32 v177, v84, v177
	v_add_f32_e32 v177, v85, v177
	v_add_f32_e32 v177, v86, v177
	v_add_f32_e32 v177, v87, v177
	v_add_f32_e32 v177, v88, v177
	v_add_f32_e32 v177, v89, v177
	v_add_f32_e32 v177, v90, v177
	v_add_f32_e32 v177, v91, v177
	v_add_f32_e32 v177, v92, v177
	v_add_f32_e32 v177, v93, v177
	v_add_f32_e32 v177, v94, v177
	v_add_f32_e32 v177, v95, v177
	v_add_f32_e32 v177, v0, v177
	v_add_f32_e32 v177, v1, v177
	v_add_f32_e32 v177, v2, v177
	v_add_f32_e32 v177, v3, v177
	v_add_f32_e32 v177, v4, v177
	v_add_f32_e32 v177, v5, v177
	v_add_f32_e32 v177, v6, v177
	v_add_f32_e32 v177, v7, v177
	v_add_f32_e32 v177, v8, v177
	v_add_f32_e32 v177, v9, v177
	v_add_f32_e32 v177, v10, v177
	v_add_f32_e32 v177, v11, v177
	v_add_f32_e32 v177, v12, v177
	v_add_f32_e32 v177, v13, v177
	v_add_f32_e32 v177, v14, v177
	v_add_f32_e32 v177, v15, v177
	v_cmp_lt_f32_e32 vcc, s36, v177
	s_nop 4
	s_cbranch_vccnz .Lmy_rare_4
.Lmy_back_4:
	ds_read_b64_tr_b16 v[54:55], v181 offset:49152
	ds_read_b64_tr_b16 v[56:57], v181 offset:49664
	v_add_f32_e32 v49, v80, v81
	v_cvt_pk_f16_f32 v50, v80, v81
	v_cvt_pk_f16_f32 v51, v82, v83
	v_cvt_pk_f16_f32 v52, v84, v85
	v_cvt_pk_f16_f32 v53, v86, v87
	ds_read_b64_tr_b16 v[58:59], v181 offset:50176
	ds_read_b64_tr_b16 v[60:61], v181 offset:50688
	s_waitcnt lgkmcnt(2)
	v_mfma_f32_32x32x16_f16 v[16:31], v[50:53], v[54:57], v[16:31]
	ds_read_b64_tr_b16 v[54:55], v181 offset:53248
	ds_read_b64_tr_b16 v[56:57], v181 offset:53760
	v_add_f32_e32 v49, v82, v49
	v_add_f32_e32 v49, v83, v49
	v_add_f32_e32 v49, v84, v49
	v_add_f32_e32 v49, v85, v49
	v_add_f32_e32 v49, v86, v49
	v_add_f32_e32 v49, v87, v49
	s_waitcnt lgkmcnt(0)
	v_mfma_f32_32x32x16_f16 v[32:47], v[50:53], v[54:57], v[32:47]
	v_add_f32_e32 v49, v88, v49
	v_add_f32_e32 v49, v89, v49
	ds_read_b64_tr_b16 v[62:63], v181 offset:54272
	ds_read_b64_tr_b16 v[64:65], v181 offset:54784
	v_add_f32_e32 v49, v90, v49
	v_add_f32_e32 v49, v91, v49
	v_cvt_pk_f16_f32 v50, v88, v89
	v_cvt_pk_f16_f32 v51, v90, v91
	v_cvt_pk_f16_f32 v52, v92, v93
	v_cvt_pk_f16_f32 v53, v94, v95
	v_add_f32_e32 v49, v92, v49
	v_mfma_f32_32x32x16_f16 v[16:31], v[50:53], v[58:61], v[16:31]
	v_add_f32_e32 v49, v93, v49
	v_add_f32_e32 v49, v94, v49
	v_add_f32_e32 v49, v95, v49
	v_add_f32_e32 v49, v0, v49
	v_add_f32_e32 v49, v1, v49
	v_add_f32_e32 v49, v2, v49
	v_add_f32_e32 v49, v3, v49
	s_waitcnt lgkmcnt(0)
	v_mfma_f32_32x32x16_f16 v[32:47], v[50:53], v[62:65], v[32:47]
	ds_read_b64_tr_b16 v[50:51], v181 offset:51200
	ds_read_b64_tr_b16 v[52:53], v181 offset:51712
	v_cvt_pk_f16_f32 v0, v0, v1
	v_cvt_pk_f16_f32 v1, v2, v3
	v_cvt_pk_f16_f32 v2, v4, v5
	v_cvt_pk_f16_f32 v3, v6, v7
	ds_read_b64_tr_b16 v[54:55], v181 offset:52224
	ds_read_b64_tr_b16 v[56:57], v181 offset:52736
	v_add_f32_e32 v4, v4, v49
	s_waitcnt lgkmcnt(2)
	v_mfma_f32_32x32x16_f16 v[16:31], v[0:3], v[50:53], v[16:31]
	ds_read_b64_tr_b16 v[50:51], v181 offset:55296
	ds_read_b64_tr_b16 v[52:53], v181 offset:55808
	v_add_f32_e32 v4, v5, v4
	v_add_f32_e32 v4, v6, v4
	ds_read_b64_tr_b16 v[58:59], v181 offset:56320
	ds_read_b64_tr_b16 v[60:61], v181 offset:56832
	v_cvt_pk_f16_f32 v5, v14, v15
	s_waitcnt lgkmcnt(2)
	v_mfma_f32_32x32x16_f16 v[32:47], v[0:3], v[50:53], v[32:47]
	v_add_f32_e32 v0, v7, v4
	v_add_f32_e32 v0, v8, v0
	v_add_f32_e32 v0, v9, v0
	v_add_f32_e32 v0, v10, v0
	v_cvt_pk_f16_f32 v2, v8, v9
	v_cvt_pk_f16_f32 v3, v10, v11
	v_cvt_pk_f16_f32 v4, v12, v13
	v_add_f32_e32 v0, v11, v0
	v_mfma_f32_32x32x16_f16 v[16:31], v[2:5], v[54:57], v[16:31]
	v_add_f32_e32 v0, v12, v0
	v_add_f32_e32 v0, v13, v0
	v_add_f32_e32 v0, v14, v0
	v_add_f32_e32 v0, v15, v0
	v_add_f32_e32 v0, v176, v0
	v_mov_b32_e32 v1, v0
	s_nop 1
	v_permlane32_swap_b32_e32 v0, v1
	s_waitcnt lgkmcnt(0)
	v_mfma_f32_32x32x16_f16 v[32:47], v[2:5], v[58:61], v[32:47]
	s_and_saveexec_b64 s[2:3], s[0:1]
	v_add_f32_e32 v0, v0, v1
	ds_write_b32 v186, v0 offset:57472
	s_or_b64 exec, exec, s[2:3]
	s_waitcnt lgkmcnt(0)
	ds_read_b128 v[0:3], v48 offset:57472
	ds_read_b128 v[4:7], v48 offset:57504
	s_mov_b32 s11, 0
	s_lshl_b64 s[0:1], s[10:11], 22
	s_add_u32 s0, s8, s0
	s_waitcnt lgkmcnt(1)
	v_rcp_f32_e32 v8, v0
	v_rcp_f32_e32 v9, v1
	s_addc_u32 s1, s9, s1
	s_lshl_b32 s2, s23, 12
	v_rcp_f32_e32 v10, v2
	v_rcp_f32_e32 v11, v3
	s_waitcnt lgkmcnt(0)
	v_rcp_f32_e32 v12, v4
	ds_read_b128 v[0:3], v48 offset:57536
	v_rcp_f32_e32 v13, v5
	v_rcp_f32_e32 v14, v6
	v_rcp_f32_e32 v15, v7
	ds_read_b128 v[4:7], v48 offset:57568
	s_add_i32 s6, s2, 0
	v_lshlrev_b32_e32 v48, 1, v189
	v_add3_u32 v48, s6, v191, v48
	v_fma_mixlo_f16 v16, v16, v8, 0
	v_fma_mixlo_f16 v8, v32, v8, 0
	ds_write_b16 v48, v8 offset:59456
	v_fma_mixlo_f16 v8, v17, v9, 0
	ds_write_b16 v48, v8 offset:59520
	v_fma_mixlo_f16 v8, v33, v9, 0
	ds_write_b16 v48, v8 offset:59584
	v_fma_mixlo_f16 v8, v18, v10, 0
	ds_write_b16 v48, v8 offset:59648
	v_fma_mixlo_f16 v8, v34, v10, 0
	ds_write_b16 v48, v8 offset:59712
	v_fma_mixlo_f16 v8, v19, v11, 0
	ds_write_b16 v48, v8 offset:59776
	v_fma_mixlo_f16 v8, v35, v11, 0
	ds_write_b16 v48, v8 offset:59840
	v_fma_mixlo_f16 v8, v20, v12, 0
	ds_write_b16 v48, v8 offset:60416
	v_fma_mixlo_f16 v8, v36, v12, 0
	ds_write_b16 v48, v8 offset:60480
	v_fma_mixlo_f16 v8, v21, v13, 0
	ds_write_b16 v48, v8 offset:60544
	v_fma_mixlo_f16 v8, v37, v13, 0
	s_waitcnt lgkmcnt(11)
	v_rcp_f32_e32 v0, v0
	ds_write_b16 v48, v8 offset:60608
	v_fma_mixlo_f16 v8, v22, v14, 0
	v_rcp_f32_e32 v1, v1
	ds_write_b16 v48, v8 offset:60672
	v_fma_mixlo_f16 v8, v38, v14, 0
	ds_write_b16 v48, v8 offset:60736
	v_fma_mixlo_f16 v8, v23, v15, 0
	v_rcp_f32_e32 v2, v2
	ds_write_b16 v48, v8 offset:60800
	v_fma_mixlo_f16 v8, v39, v15, 0
	ds_write_b16 v48, v8 offset:60864
	v_fma_mixlo_f16 v8, v24, v0, 0
	v_fma_mixlo_f16 v0, v40, v0, 0
	v_rcp_f32_e32 v3, v3
	ds_write_b16 v48, v0 offset:61504
	v_fma_mixlo_f16 v0, v25, v1, 0
	ds_write_b16 v48, v0 offset:61568
	v_fma_mixlo_f16 v0, v41, v1, 0
	s_waitcnt lgkmcnt(14)
	v_rcp_f32_e32 v4, v4
	ds_write_b16 v48, v0 offset:61632
	v_fma_mixlo_f16 v0, v26, v2, 0
	ds_write_b16 v48, v0 offset:61696
	v_fma_mixlo_f16 v0, v42, v2, 0
	v_rcp_f32_e32 v5, v5
	ds_write_b16 v48, v0 offset:61760
	v_fma_mixlo_f16 v0, v27, v3, 0
	ds_write_b16 v48, v0 offset:61824
	v_fma_mixlo_f16 v0, v43, v3, 0
	v_rcp_f32_e32 v6, v6
	ds_write_b16 v48, v0 offset:61888
	v_fma_mixlo_f16 v0, v28, v4, 0
	ds_write_b16 v48, v0 offset:62464
	v_fma_mixlo_f16 v0, v44, v4, 0
	v_rcp_f32_e32 v7, v7
	ds_write_b16 v48, v0 offset:62528
	v_fma_mixlo_f16 v0, v29, v5, 0
	ds_write_b16 v48, v0 offset:62592
	v_fma_mixlo_f16 v0, v45, v5, 0
	ds_write_b16 v48, v0 offset:62656
	v_fma_mixlo_f16 v0, v30, v6, 0
	ds_write_b16 v48, v0 offset:62720
	v_fma_mixlo_f16 v0, v46, v6, 0
	ds_write_b16 v48, v0 offset:62784
	v_fma_mixlo_f16 v0, v31, v7, 0
	ds_write_b16 v48, v0 offset:62848
	v_fma_mixlo_f16 v0, v47, v7, 0
	ds_write_b16 v48, v0 offset:62912
	v_lshrrev_b32_e32 v0, 3, v188
	v_and_b32_e32 v4, 56, v190
	s_lshl_b32 s4, s24, 8
	s_lshl_b32 s5, s22, 9
	ds_write_b16 v48, v16 offset:59392
	ds_write_b16 v48, v8 offset:61440
	v_lshlrev_b32_e32 v1, 7, v0
	v_lshlrev_b32_e32 v2, 1, v4
	s_waitcnt lgkmcnt(0)
	v_add3_u32 v8, s6, v1, v2
	s_or_b32 s4, s4, s5
	v_or_b32_e32 v5, s4, v0
	ds_read_b128 v[0:3], v8 offset:59392
	s_lshl_b32 s7, s20, 6
	v_add_lshl_u32 v5, v5, s21, 8
	v_or3_b32 v4, v5, s7, v4
	s_and_b32 s1, s1, 0xffff
	s_mov_b32 s3, 0x20000
	s_mov_b32 s2, 0x400000
	v_lshlrev_b32_e32 v12, 1, v4
	ds_read_b128 v[4:7], v8 offset:60416
	s_waitcnt lgkmcnt(1)
	buffer_store_dwordx4 v[0:3], v12, s[0:3], 0 offen sc1
	ds_read_b128 v[0:3], v8 offset:61440
	ds_read_b128 v[8:11], v8 offset:62464
	v_add_u32_e32 v13, 0x1000, v12
	s_waitcnt lgkmcnt(2)
	buffer_store_dwordx4 v[4:7], v13, s[0:3], 0 offen sc1
	s_nop 1
	v_add_u32_e32 v4, 0x2000, v12
	s_waitcnt lgkmcnt(1)
	buffer_store_dwordx4 v[0:3], v4, s[0:3], 0 offen sc1
	s_nop 1
	v_add_u32_e32 v0, 0x3000, v12
	s_waitcnt lgkmcnt(0)
	buffer_store_dwordx4 v[8:11], v0, s[0:3], 0 offen sc1
	s_waitcnt lgkmcnt(0)
	s_barrier
	s_endpgm
.Lmy_rare_1:
	s_sub_u32 s38, s44, s25
	s_subb_u32 s39, s45, 0
	s_sub_u32 s38, s38, 0xa000
	s_subb_u32 s39, s39, 0
	s_add_u32 s48, s38, 0x1000
	s_addc_u32 s49, s39, 0
	v_lshlrev_b32_e32 v160, 4, v189
	v_lshl_add_u32 v160, v191, 1, v160
	v_xor_b32_e32 v166, 0x80000000, v183
	s_lshl_b32 s42, s23, 12
	v_lshlrev_b32_e32 v167, 2, v188
	v_add_u32_e32 v167, s42, v167
	global_load_dwordx4 v[140:143], v160, s[38:39]
	global_load_dwordx4 v[132:135], v160, s[38:39] offset:2048
	global_load_dwordx4 v[124:127], v160, s[48:49]
	global_load_dwordx4 v[116:119], v160, s[48:49] offset:2048
	v_mov_b32_e32 v144, v166
	v_mov_b32_e32 v145, v166
	v_mov_b32_e32 v146, v166
	v_mov_b32_e32 v147, v166
	v_mov_b32_e32 v148, v166
	v_mov_b32_e32 v149, v166
	v_mov_b32_e32 v150, v166
	v_mov_b32_e32 v151, v166
	v_mov_b32_e32 v152, v166
	v_mov_b32_e32 v153, v166
	v_mov_b32_e32 v154, v166
	v_mov_b32_e32 v155, v166
	v_mov_b32_e32 v156, v166
	v_mov_b32_e32 v157, v166
	v_mov_b32_e32 v158, v166
	v_mov_b32_e32 v159, v166
	s_waitcnt vmcnt(0)
	s_nop 1
	v_mfma_f32_32x32x16_f16 v[144:159], v[140:143], v[136:139], v[144:159]
	v_mfma_f32_32x32x16_f16 v[144:159], v[132:135], v[128:131], v[144:159]
	v_mfma_f32_32x32x16_f16 v[144:159], v[124:127], v[120:123], v[144:159]
	v_mfma_f32_32x32x16_f16 v[144:159], v[116:119], v[112:115], v[144:159]
	s_nop 15
	s_nop 3
	v_max3_f32 v164, v144, v145, v146
	v_max3_f32 v164, v164, v147, v148
	v_max3_f32 v164, v164, v149, v150
	v_max3_f32 v164, v164, v151, v152
	v_max3_f32 v164, v164, v153, v154
	v_max3_f32 v164, v164, v155, v156
	v_max3_f32 v164, v164, v157, v158
	v_max_f32_e32 v164, v164, v159
	ds_write_b32 v167, v144 offset:59392
	ds_write_b32 v167, v145 offset:59648
	ds_write_b32 v167, v146 offset:59904
	ds_write_b32 v167, v147 offset:60160
	ds_write_b32 v167, v148 offset:60416
	ds_write_b32 v167, v149 offset:60672
	ds_write_b32 v167, v150 offset:60928
	ds_write_b32 v167, v151 offset:61184
	ds_write_b32 v167, v152 offset:61440
	ds_write_b32 v167, v153 offset:61696
	ds_write_b32 v167, v154 offset:61952
	ds_write_b32 v167, v155 offset:62208
	ds_write_b32 v167, v156 offset:62464
	ds_write_b32 v167, v157 offset:62720
	ds_write_b32 v167, v158 offset:62976
	ds_write_b32 v167, v159 offset:63232
	s_waitcnt lgkmcnt(0)
	global_load_dwordx4 v[140:143], v160, s[38:39] offset:512
	global_load_dwordx4 v[132:135], v160, s[38:39] offset:2560
	global_load_dwordx4 v[124:127], v160, s[48:49] offset:512
	global_load_dwordx4 v[116:119], v160, s[48:49] offset:2560
	v_mov_b32_e32 v144, v166
	v_mov_b32_e32 v145, v166
	v_mov_b32_e32 v146, v166
	v_mov_b32_e32 v147, v166
	v_mov_b32_e32 v148, v166
	v_mov_b32_e32 v149, v166
	v_mov_b32_e32 v150, v166
	v_mov_b32_e32 v151, v166
	v_mov_b32_e32 v152, v166
	v_mov_b32_e32 v153, v166
	v_mov_b32_e32 v154, v166
	v_mov_b32_e32 v155, v166
	v_mov_b32_e32 v156, v166
	v_mov_b32_e32 v157, v166
	v_mov_b32_e32 v158, v166
	v_mov_b32_e32 v159, v166
	s_waitcnt vmcnt(0)
	s_nop 1
	v_mfma_f32_32x32x16_f16 v[144:159], v[140:143], v[136:139], v[144:159]
	v_mfma_f32_32x32x16_f16 v[144:159], v[132:135], v[128:131], v[144:159]
	v_mfma_f32_32x32x16_f16 v[144:159], v[124:127], v[120:123], v[144:159]
	v_mfma_f32_32x32x16_f16 v[144:159], v[116:119], v[112:115], v[144:159]
	s_nop 15
	s_nop 3
	v_max3_f32 v165, v144, v145, v146
	v_max3_f32 v165, v165, v147, v148
	v_max3_f32 v165, v165, v149, v150
	v_max3_f32 v165, v165, v151, v152
	v_max3_f32 v165, v165, v153, v154
	v_max3_f32 v165, v165, v155, v156
	v_max3_f32 v165, v165, v157, v158
	v_max_f32_e32 v165, v165, v159
	v_max_f32_e32 v164, v164, v165
	v_mov_b32_e32 v165, v164
	s_nop 1
	v_permlane32_swap_b32_e32 v164, v165
	v_max_f32_e32 v164, v165, v164
	s_mov_b32 s37, 0x41000000
	v_cmp_lt_f32_e32 vcc, s37, v164
	v_max_f32_e32 v164, 0, v164
	s_nop 4
	s_cbranch_vccnz .Lmy_rare_1_rs
	v_mov_b32_e32 v164, 0
	s_branch .Lmy_rare_1_nr
.Lmy_rare_1_rs:
	v_add_f32_e32 v183, v183, v164
	v_exp_f32_e64 v165, -v164
	v_sub_f32_e32 v96, v96, v164
	v_sub_f32_e32 v97, v97, v164
	v_sub_f32_e32 v98, v98, v164
	v_sub_f32_e32 v99, v99, v164
	v_sub_f32_e32 v100, v100, v164
	v_sub_f32_e32 v101, v101, v164
	v_sub_f32_e32 v102, v102, v164
	v_sub_f32_e32 v103, v103, v164
	v_sub_f32_e32 v104, v104, v164
	v_sub_f32_e32 v105, v105, v164
	v_sub_f32_e32 v106, v106, v164
	v_sub_f32_e32 v107, v107, v164
	v_sub_f32_e32 v108, v108, v164
	v_sub_f32_e32 v109, v109, v164
	v_sub_f32_e32 v110, v110, v164
	v_sub_f32_e32 v111, v111, v164
	v_sub_f32_e32 v80, v80, v164
	v_sub_f32_e32 v81, v81, v164
	v_sub_f32_e32 v82, v82, v164
	v_sub_f32_e32 v83, v83, v164
	v_sub_f32_e32 v84, v84, v164
	v_sub_f32_e32 v85, v85, v164
	v_sub_f32_e32 v86, v86, v164
	v_sub_f32_e32 v87, v87, v164
	v_sub_f32_e32 v88, v88, v164
	v_sub_f32_e32 v89, v89, v164
	v_sub_f32_e32 v90, v90, v164
	v_sub_f32_e32 v91, v91, v164
	v_sub_f32_e32 v92, v92, v164
	v_sub_f32_e32 v93, v93, v164
	v_sub_f32_e32 v94, v94, v164
	v_sub_f32_e32 v95, v95, v164
	v_xor_b32_e32 v0, 0x80000000, v183
	v_mov_b32_e32 v1, v0
	v_mov_b32_e32 v2, v0
	v_mov_b32_e32 v3, v0
	v_mov_b32_e32 v4, v0
	v_mov_b32_e32 v5, v0
	v_mov_b32_e32 v6, v0
	v_mov_b32_e32 v7, v0
	v_mov_b32_e32 v8, v0
	v_mov_b32_e32 v9, v0
	v_mov_b32_e32 v10, v0
	v_mov_b32_e32 v11, v0
	v_mov_b32_e32 v12, v0
	v_mov_b32_e32 v13, v0
	v_mov_b32_e32 v14, v0
	v_mov_b32_e32 v15, v0
	v_mul_f32_e32 v187, v187, v165
	s_and_saveexec_b64 s[40:41], s[0:1]
	ds_write_b32 v186, v165 offset:57344
	s_or_b64 exec, exec, s[40:41]
	v_add_u32_e32 v166, s11, v182
	s_waitcnt lgkmcnt(0)
	ds_read_b128 v[140:143], v166 offset:57344
	ds_read_b128 v[132:135], v166 offset:57376
	ds_read_b128 v[124:127], v166 offset:57408
	ds_read_b128 v[116:119], v166 offset:57440
	s_waitcnt lgkmcnt(0)
	v_pk_mul_f32 v[16:17], v[16:17], v[140:141]
	v_pk_mul_f32 v[32:33], v[32:33], v[140:141]
	v_pk_mul_f32 v[18:19], v[18:19], v[142:143]
	v_pk_mul_f32 v[34:35], v[34:35], v[142:143]
	v_pk_mul_f32 v[20:21], v[20:21], v[132:133]
	v_pk_mul_f32 v[36:37], v[36:37], v[132:133]
	v_pk_mul_f32 v[22:23], v[22:23], v[134:135]
	v_pk_mul_f32 v[38:39], v[38:39], v[134:135]
	v_pk_mul_f32 v[24:25], v[24:25], v[124:125]
	v_pk_mul_f32 v[40:41], v[40:41], v[124:125]
	v_pk_mul_f32 v[26:27], v[26:27], v[126:127]
	v_pk_mul_f32 v[42:43], v[42:43], v[126:127]
	v_pk_mul_f32 v[28:29], v[28:29], v[116:117]
	v_pk_mul_f32 v[44:45], v[44:45], v[116:117]
	v_pk_mul_f32 v[30:31], v[30:31], v[118:119]
	v_pk_mul_f32 v[46:47], v[46:47], v[118:119]

.Lmy_rare_2:
	s_sub_u32 s38, s44, s25
	s_subb_u32 s39, s45, 0
	s_sub_u32 s38, s38, 0xa000
	s_subb_u32 s39, s39, 0
	s_add_u32 s48, s38, 0x1000
	s_addc_u32 s49, s39, 0
	v_lshlrev_b32_e32 v172, 4, v189
	v_lshl_add_u32 v172, v191, 1, v172
	v_xor_b32_e32 v178, 0x80000000, v183
	s_lshl_b32 s42, s23, 12
	v_lshlrev_b32_e32 v179, 2, v188
	v_add_u32_e32 v179, s42, v179
	global_load_dwordx4 v[140:143], v172, s[38:39]
	global_load_dwordx4 v[132:135], v172, s[38:39] offset:2048
	global_load_dwordx4 v[124:127], v172, s[48:49]
	global_load_dwordx4 v[116:119], v172, s[48:49] offset:2048
	v_mov_b32_e32 v156, v178
	v_mov_b32_e32 v157, v178
	v_mov_b32_e32 v158, v178
	v_mov_b32_e32 v159, v178
	v_mov_b32_e32 v160, v178
	v_mov_b32_e32 v161, v178
	v_mov_b32_e32 v162, v178
	v_mov_b32_e32 v163, v178
	v_mov_b32_e32 v164, v178
	v_mov_b32_e32 v165, v178
	v_mov_b32_e32 v166, v178
	v_mov_b32_e32 v167, v178
	v_mov_b32_e32 v168, v178
	v_mov_b32_e32 v169, v178
	v_mov_b32_e32 v170, v178
	v_mov_b32_e32 v171, v178
	s_waitcnt vmcnt(0)
	s_nop 1
	v_mfma_f32_32x32x16_f16 v[156:171], v[140:143], v[136:139], v[156:171]
	v_mfma_f32_32x32x16_f16 v[156:171], v[132:135], v[128:131], v[156:171]
	v_mfma_f32_32x32x16_f16 v[156:171], v[124:127], v[120:123], v[156:171]
	v_mfma_f32_32x32x16_f16 v[156:171], v[116:119], v[112:115], v[156:171]
	s_nop 15
	s_nop 3
	v_max3_f32 v176, v156, v157, v158
	v_max3_f32 v176, v176, v159, v160
	v_max3_f32 v176, v176, v161, v162
	v_max3_f32 v176, v176, v163, v164
	v_max3_f32 v176, v176, v165, v166
	v_max3_f32 v176, v176, v167, v168
	v_max3_f32 v176, v176, v169, v170
	v_max_f32_e32 v176, v176, v171
	ds_write_b32 v179, v156 offset:59392
	ds_write_b32 v179, v157 offset:59648
	ds_write_b32 v179, v158 offset:59904
	ds_write_b32 v179, v159 offset:60160
	ds_write_b32 v179, v160 offset:60416
	ds_write_b32 v179, v161 offset:60672
	ds_write_b32 v179, v162 offset:60928
	ds_write_b32 v179, v163 offset:61184
	ds_write_b32 v179, v164 offset:61440
	ds_write_b32 v179, v165 offset:61696
	ds_write_b32 v179, v166 offset:61952
	ds_write_b32 v179, v167 offset:62208
	ds_write_b32 v179, v168 offset:62464
	ds_write_b32 v179, v169 offset:62720
	ds_write_b32 v179, v170 offset:62976
	ds_write_b32 v179, v171 offset:63232
	s_waitcnt lgkmcnt(0)
	global_load_dwordx4 v[140:143], v172, s[38:39] offset:512
	global_load_dwordx4 v[132:135], v172, s[38:39] offset:2560
	global_load_dwordx4 v[124:127], v172, s[48:49] offset:512
	global_load_dwordx4 v[116:119], v172, s[48:49] offset:2560
	v_mov_b32_e32 v156, v178
	v_mov_b32_e32 v157, v178
	v_mov_b32_e32 v158, v178
	v_mov_b32_e32 v159, v178
	v_mov_b32_e32 v160, v178
	v_mov_b32_e32 v161, v178
	v_mov_b32_e32 v162, v178
	v_mov_b32_e32 v163, v178
	v_mov_b32_e32 v164, v178
	v_mov_b32_e32 v165, v178
	v_mov_b32_e32 v166, v178
	v_mov_b32_e32 v167, v178
	v_mov_b32_e32 v168, v178
	v_mov_b32_e32 v169, v178
	v_mov_b32_e32 v170, v178
	v_mov_b32_e32 v171, v178
	s_waitcnt vmcnt(0)
	s_nop 1
	v_mfma_f32_32x32x16_f16 v[156:171], v[140:143], v[136:139], v[156:171]
	v_mfma_f32_32x32x16_f16 v[156:171], v[132:135], v[128:131], v[156:171]
	v_mfma_f32_32x32x16_f16 v[156:171], v[124:127], v[120:123], v[156:171]
	v_mfma_f32_32x32x16_f16 v[156:171], v[116:119], v[112:115], v[156:171]
	s_nop 15
	s_nop 3
	v_max3_f32 v177, v156, v157, v158
	v_max3_f32 v177, v177, v159, v160
	v_max3_f32 v177, v177, v161, v162
	v_max3_f32 v177, v177, v163, v164
	v_max3_f32 v177, v177, v165, v166
	v_max3_f32 v177, v177, v167, v168
	v_max3_f32 v177, v177, v169, v170
	v_max_f32_e32 v177, v177, v171
	v_max_f32_e32 v176, v176, v177
	v_mov_b32_e32 v177, v176
	s_nop 1
	v_permlane32_swap_b32_e32 v176, v177
	v_max_f32_e32 v176, v177, v176
	s_mov_b32 s37, 0x41000000
	v_cmp_lt_f32_e32 vcc, s37, v176
	v_max_f32_e32 v176, 0, v176
	s_nop 4
	s_cbranch_vccnz .Lmy_rare_2_rs
	v_mov_b32_e32 v176, 0
	s_branch .Lmy_rare_2_nr
.Lmy_rare_2_rs:
	v_add_f32_e32 v183, v183, v176
	v_exp_f32_e64 v177, -v176
	v_sub_f32_e32 v64, v64, v176
	v_sub_f32_e32 v65, v65, v176
	v_sub_f32_e32 v66, v66, v176
	v_sub_f32_e32 v67, v67, v176
	v_sub_f32_e32 v68, v68, v176
	v_sub_f32_e32 v69, v69, v176
	v_sub_f32_e32 v70, v70, v176
	v_sub_f32_e32 v71, v71, v176
	v_sub_f32_e32 v72, v72, v176
	v_sub_f32_e32 v73, v73, v176
	v_sub_f32_e32 v74, v74, v176
	v_sub_f32_e32 v75, v75, v176
	v_sub_f32_e32 v76, v76, v176
	v_sub_f32_e32 v77, v77, v176
	v_sub_f32_e32 v78, v78, v176
	v_sub_f32_e32 v79, v79, v176
	v_sub_f32_e32 v48, v48, v176
	v_sub_f32_e32 v49, v49, v176
	v_sub_f32_e32 v50, v50, v176
	v_sub_f32_e32 v51, v51, v176
	v_sub_f32_e32 v52, v52, v176
	v_sub_f32_e32 v53, v53, v176
	v_sub_f32_e32 v54, v54, v176
	v_sub_f32_e32 v55, v55, v176
	v_sub_f32_e32 v56, v56, v176
	v_sub_f32_e32 v57, v57, v176
	v_sub_f32_e32 v58, v58, v176
	v_sub_f32_e32 v59, v59, v176
	v_sub_f32_e32 v60, v60, v176
	v_sub_f32_e32 v61, v61, v176
	v_sub_f32_e32 v62, v62, v176
	v_sub_f32_e32 v63, v63, v176
	v_xor_b32_e32 v0, 0x80000000, v183
	v_mov_b32_e32 v1, v0
	v_mov_b32_e32 v2, v0
	v_mov_b32_e32 v3, v0
	v_mov_b32_e32 v4, v0
	v_mov_b32_e32 v5, v0
	v_mov_b32_e32 v6, v0
	v_mov_b32_e32 v7, v0
	v_mov_b32_e32 v8, v0
	v_mov_b32_e32 v9, v0
	v_mov_b32_e32 v10, v0
	v_mov_b32_e32 v11, v0
	v_mov_b32_e32 v12, v0
	v_mov_b32_e32 v13, v0
	v_mov_b32_e32 v14, v0
	v_mov_b32_e32 v15, v0
	v_mul_f32_e32 v187, v187, v177
	s_and_saveexec_b64 s[40:41], s[0:1]
	ds_write_b32 v186, v177 offset:57344
	s_or_b64 exec, exec, s[40:41]
	v_add_u32_e32 v178, s11, v182
	s_waitcnt lgkmcnt(0)
	ds_read_b128 v[140:143], v178 offset:57344
	ds_read_b128 v[132:135], v178 offset:57376
	ds_read_b128 v[124:127], v178 offset:57408
	ds_read_b128 v[116:119], v178 offset:57440
	s_waitcnt lgkmcnt(0)
	v_pk_mul_f32 v[16:17], v[16:17], v[140:141]
	v_pk_mul_f32 v[32:33], v[32:33], v[140:141]
	v_pk_mul_f32 v[18:19], v[18:19], v[142:143]
	v_pk_mul_f32 v[34:35], v[34:35], v[142:143]
	v_pk_mul_f32 v[20:21], v[20:21], v[132:133]
	v_pk_mul_f32 v[36:37], v[36:37], v[132:133]
	v_pk_mul_f32 v[22:23], v[22:23], v[134:135]
	v_pk_mul_f32 v[38:39], v[38:39], v[134:135]
	v_pk_mul_f32 v[24:25], v[24:25], v[124:125]
	v_pk_mul_f32 v[40:41], v[40:41], v[124:125]
	v_pk_mul_f32 v[26:27], v[26:27], v[126:127]
	v_pk_mul_f32 v[42:43], v[42:43], v[126:127]
	v_pk_mul_f32 v[28:29], v[28:29], v[116:117]
	v_pk_mul_f32 v[44:45], v[44:45], v[116:117]
	v_pk_mul_f32 v[30:31], v[30:31], v[118:119]
	v_pk_mul_f32 v[46:47], v[46:47], v[118:119]

.Lmy_rare_3:
	s_sub_u32 s38, s44, s25
	s_subb_u32 s39, s45, 0
	s_sub_u32 s38, s38, 0x8000
	s_subb_u32 s39, s39, 0
	s_add_u32 s48, s38, 0x1000
	s_addc_u32 s49, s39, 0
	v_lshlrev_b32_e32 v160, 4, v189
	v_lshl_add_u32 v160, v191, 1, v160
	v_xor_b32_e32 v166, 0x80000000, v183
	s_lshl_b32 s42, s23, 12
	v_lshlrev_b32_e32 v167, 2, v188
	v_add_u32_e32 v167, s42, v167
	global_load_dwordx4 v[140:143], v160, s[38:39]
	global_load_dwordx4 v[132:135], v160, s[38:39] offset:2048
	global_load_dwordx4 v[124:127], v160, s[48:49]
	global_load_dwordx4 v[116:119], v160, s[48:49] offset:2048
	v_mov_b32_e32 v144, v166
	v_mov_b32_e32 v145, v166
	v_mov_b32_e32 v146, v166
	v_mov_b32_e32 v147, v166
	v_mov_b32_e32 v148, v166
	v_mov_b32_e32 v149, v166
	v_mov_b32_e32 v150, v166
	v_mov_b32_e32 v151, v166
	v_mov_b32_e32 v152, v166
	v_mov_b32_e32 v153, v166
	v_mov_b32_e32 v154, v166
	v_mov_b32_e32 v155, v166
	v_mov_b32_e32 v156, v166
	v_mov_b32_e32 v157, v166
	v_mov_b32_e32 v158, v166
	v_mov_b32_e32 v159, v166
	s_waitcnt vmcnt(0)
	s_nop 1
	v_mfma_f32_32x32x16_f16 v[144:159], v[140:143], v[136:139], v[144:159]
	v_mfma_f32_32x32x16_f16 v[144:159], v[132:135], v[128:131], v[144:159]
	v_mfma_f32_32x32x16_f16 v[144:159], v[124:127], v[120:123], v[144:159]
	v_mfma_f32_32x32x16_f16 v[144:159], v[116:119], v[112:115], v[144:159]
	s_nop 15
	s_nop 3
	v_max3_f32 v164, v144, v145, v146
	v_max3_f32 v164, v164, v147, v148
	v_max3_f32 v164, v164, v149, v150
	v_max3_f32 v164, v164, v151, v152
	v_max3_f32 v164, v164, v153, v154
	v_max3_f32 v164, v164, v155, v156
	v_max3_f32 v164, v164, v157, v158
	v_max_f32_e32 v164, v164, v159
	ds_write_b32 v167, v144 offset:59392
	ds_write_b32 v167, v145 offset:59648
	ds_write_b32 v167, v146 offset:59904
	ds_write_b32 v167, v147 offset:60160
	ds_write_b32 v167, v148 offset:60416
	ds_write_b32 v167, v149 offset:60672
	ds_write_b32 v167, v150 offset:60928
	ds_write_b32 v167, v151 offset:61184
	ds_write_b32 v167, v152 offset:61440
	ds_write_b32 v167, v153 offset:61696
	ds_write_b32 v167, v154 offset:61952
	ds_write_b32 v167, v155 offset:62208
	ds_write_b32 v167, v156 offset:62464
	ds_write_b32 v167, v157 offset:62720
	ds_write_b32 v167, v158 offset:62976
	ds_write_b32 v167, v159 offset:63232
	s_waitcnt lgkmcnt(0)
	global_load_dwordx4 v[140:143], v160, s[38:39] offset:512
	global_load_dwordx4 v[132:135], v160, s[38:39] offset:2560
	global_load_dwordx4 v[124:127], v160, s[48:49] offset:512
	global_load_dwordx4 v[116:119], v160, s[48:49] offset:2560
	v_mov_b32_e32 v144, v166
	v_mov_b32_e32 v145, v166
	v_mov_b32_e32 v146, v166
	v_mov_b32_e32 v147, v166
	v_mov_b32_e32 v148, v166
	v_mov_b32_e32 v149, v166
	v_mov_b32_e32 v150, v166
	v_mov_b32_e32 v151, v166
	v_mov_b32_e32 v152, v166
	v_mov_b32_e32 v153, v166
	v_mov_b32_e32 v154, v166
	v_mov_b32_e32 v155, v166
	v_mov_b32_e32 v156, v166
	v_mov_b32_e32 v157, v166
	v_mov_b32_e32 v158, v166
	v_mov_b32_e32 v159, v166
	s_waitcnt vmcnt(0)
	s_nop 1
	v_mfma_f32_32x32x16_f16 v[144:159], v[140:143], v[136:139], v[144:159]
	v_mfma_f32_32x32x16_f16 v[144:159], v[132:135], v[128:131], v[144:159]
	v_mfma_f32_32x32x16_f16 v[144:159], v[124:127], v[120:123], v[144:159]
	v_mfma_f32_32x32x16_f16 v[144:159], v[116:119], v[112:115], v[144:159]
	s_nop 15
	s_nop 3
	v_max3_f32 v165, v144, v145, v146
	v_max3_f32 v165, v165, v147, v148
	v_max3_f32 v165, v165, v149, v150
	v_max3_f32 v165, v165, v151, v152
	v_max3_f32 v165, v165, v153, v154
	v_max3_f32 v165, v165, v155, v156
	v_max3_f32 v165, v165, v157, v158
	v_max_f32_e32 v165, v165, v159
	v_max_f32_e32 v164, v164, v165
	v_mov_b32_e32 v165, v164
	s_nop 1
	v_permlane32_swap_b32_e32 v164, v165
	v_max_f32_e32 v164, v165, v164
	s_mov_b32 s37, 0x41000000
	v_cmp_lt_f32_e32 vcc, s37, v164
	v_max_f32_e32 v164, 0, v164
	s_nop 4
	s_cbranch_vccnz .Lmy_rare_3_rs
	v_mov_b32_e32 v164, 0
	s_branch .Lmy_rare_3_nr
.Lmy_rare_3_rs:
	v_add_f32_e32 v183, v183, v164
	v_exp_f32_e64 v165, -v164
	v_sub_f32_e32 v80, v80, v164
	v_sub_f32_e32 v81, v81, v164
	v_sub_f32_e32 v82, v82, v164
	v_sub_f32_e32 v83, v83, v164
	v_sub_f32_e32 v84, v84, v164
	v_sub_f32_e32 v85, v85, v164
	v_sub_f32_e32 v86, v86, v164
	v_sub_f32_e32 v87, v87, v164
	v_sub_f32_e32 v88, v88, v164
	v_sub_f32_e32 v89, v89, v164
	v_sub_f32_e32 v90, v90, v164
	v_sub_f32_e32 v91, v91, v164
	v_sub_f32_e32 v92, v92, v164
	v_sub_f32_e32 v93, v93, v164
	v_sub_f32_e32 v94, v94, v164
	v_sub_f32_e32 v95, v95, v164
	v_sub_f32_e32 v0, v0, v164
	v_sub_f32_e32 v1, v1, v164
	v_sub_f32_e32 v2, v2, v164
	v_sub_f32_e32 v3, v3, v164
	v_sub_f32_e32 v4, v4, v164
	v_sub_f32_e32 v5, v5, v164
	v_sub_f32_e32 v6, v6, v164
	v_sub_f32_e32 v7, v7, v164
	v_sub_f32_e32 v8, v8, v164
	v_sub_f32_e32 v9, v9, v164
	v_sub_f32_e32 v10, v10, v164
	v_sub_f32_e32 v11, v11, v164
	v_sub_f32_e32 v12, v12, v164
	v_sub_f32_e32 v13, v13, v164
	v_sub_f32_e32 v14, v14, v164
	v_sub_f32_e32 v15, v15, v164
	v_mul_f32_e32 v187, v187, v165
	s_and_saveexec_b64 s[40:41], s[0:1]
	ds_write_b32 v186, v165 offset:57344
	s_or_b64 exec, exec, s[40:41]
	v_add_u32_e32 v166, s11, v182
	s_waitcnt lgkmcnt(0)
	ds_read_b128 v[140:143], v166 offset:57344
	ds_read_b128 v[132:135], v166 offset:57376
	ds_read_b128 v[124:127], v166 offset:57408
	ds_read_b128 v[116:119], v166 offset:57440
	s_waitcnt lgkmcnt(0)
	v_pk_mul_f32 v[16:17], v[16:17], v[140:141]
	v_pk_mul_f32 v[32:33], v[32:33], v[140:141]
	v_pk_mul_f32 v[18:19], v[18:19], v[142:143]
	v_pk_mul_f32 v[34:35], v[34:35], v[142:143]
	v_pk_mul_f32 v[20:21], v[20:21], v[132:133]
	v_pk_mul_f32 v[36:37], v[36:37], v[132:133]
	v_pk_mul_f32 v[22:23], v[22:23], v[134:135]
	v_pk_mul_f32 v[38:39], v[38:39], v[134:135]
	v_pk_mul_f32 v[24:25], v[24:25], v[124:125]
	v_pk_mul_f32 v[40:41], v[40:41], v[124:125]
	v_pk_mul_f32 v[26:27], v[26:27], v[126:127]
	v_pk_mul_f32 v[42:43], v[42:43], v[126:127]
	v_pk_mul_f32 v[28:29], v[28:29], v[116:117]
	v_pk_mul_f32 v[44:45], v[44:45], v[116:117]
	v_pk_mul_f32 v[30:31], v[30:31], v[118:119]
	v_pk_mul_f32 v[46:47], v[46:47], v[118:119]

.Lmy_rare_4:
	s_sub_u32 s38, s44, s25
	s_subb_u32 s39, s45, 0
	s_sub_u32 s38, s38, 0x6000
	s_subb_u32 s39, s39, 0
	s_add_u32 s48, s38, 0x1000
	s_addc_u32 s49, s39, 0
	v_lshlrev_b32_e32 v160, 4, v189
	v_lshl_add_u32 v160, v191, 1, v160
	v_xor_b32_e32 v166, 0x80000000, v183
	s_lshl_b32 s42, s23, 12
	v_lshlrev_b32_e32 v167, 2, v188
	v_add_u32_e32 v167, s42, v167
	global_load_dwordx4 v[140:143], v160, s[38:39]
	global_load_dwordx4 v[132:135], v160, s[38:39] offset:2048
	global_load_dwordx4 v[124:127], v160, s[48:49]
	global_load_dwordx4 v[116:119], v160, s[48:49] offset:2048
	v_mov_b32_e32 v144, v166
	v_mov_b32_e32 v145, v166
	v_mov_b32_e32 v146, v166
	v_mov_b32_e32 v147, v166
	v_mov_b32_e32 v148, v166
	v_mov_b32_e32 v149, v166
	v_mov_b32_e32 v150, v166
	v_mov_b32_e32 v151, v166
	v_mov_b32_e32 v152, v166
	v_mov_b32_e32 v153, v166
	v_mov_b32_e32 v154, v166
	v_mov_b32_e32 v155, v166
	v_mov_b32_e32 v156, v166
	v_mov_b32_e32 v157, v166
	v_mov_b32_e32 v158, v166
	v_mov_b32_e32 v159, v166
	s_waitcnt vmcnt(0)
	s_nop 1
	v_mfma_f32_32x32x16_f16 v[144:159], v[140:143], v[136:139], v[144:159]
	v_mfma_f32_32x32x16_f16 v[144:159], v[132:135], v[128:131], v[144:159]
	v_mfma_f32_32x32x16_f16 v[144:159], v[124:127], v[120:123], v[144:159]
	v_mfma_f32_32x32x16_f16 v[144:159], v[116:119], v[112:115], v[144:159]
	s_nop 15
	s_nop 3
	v_max3_f32 v164, v144, v145, v146
	v_max3_f32 v164, v164, v147, v148
	v_max3_f32 v164, v164, v149, v150
	v_max3_f32 v164, v164, v151, v152
	v_max3_f32 v164, v164, v153, v154
	v_max3_f32 v164, v164, v155, v156
	v_max3_f32 v164, v164, v157, v158
	v_max_f32_e32 v164, v164, v159
	ds_write_b32 v167, v144 offset:59392
	ds_write_b32 v167, v145 offset:59648
	ds_write_b32 v167, v146 offset:59904
	ds_write_b32 v167, v147 offset:60160
	ds_write_b32 v167, v148 offset:60416
	ds_write_b32 v167, v149 offset:60672
	ds_write_b32 v167, v150 offset:60928
	ds_write_b32 v167, v151 offset:61184
	ds_write_b32 v167, v152 offset:61440
	ds_write_b32 v167, v153 offset:61696
	ds_write_b32 v167, v154 offset:61952
	ds_write_b32 v167, v155 offset:62208
	ds_write_b32 v167, v156 offset:62464
	ds_write_b32 v167, v157 offset:62720
	ds_write_b32 v167, v158 offset:62976
	ds_write_b32 v167, v159 offset:63232
	s_waitcnt lgkmcnt(0)
	global_load_dwordx4 v[140:143], v160, s[38:39] offset:512
	global_load_dwordx4 v[132:135], v160, s[38:39] offset:2560
	global_load_dwordx4 v[124:127], v160, s[48:49] offset:512
	global_load_dwordx4 v[116:119], v160, s[48:49] offset:2560
	v_mov_b32_e32 v144, v166
	v_mov_b32_e32 v145, v166
	v_mov_b32_e32 v146, v166
	v_mov_b32_e32 v147, v166
	v_mov_b32_e32 v148, v166
	v_mov_b32_e32 v149, v166
	v_mov_b32_e32 v150, v166
	v_mov_b32_e32 v151, v166
	v_mov_b32_e32 v152, v166
	v_mov_b32_e32 v153, v166
	v_mov_b32_e32 v154, v166
	v_mov_b32_e32 v155, v166
	v_mov_b32_e32 v156, v166
	v_mov_b32_e32 v157, v166
	v_mov_b32_e32 v158, v166
	v_mov_b32_e32 v159, v166
	s_waitcnt vmcnt(0)
	s_nop 1
	v_mfma_f32_32x32x16_f16 v[144:159], v[140:143], v[136:139], v[144:159]
	v_mfma_f32_32x32x16_f16 v[144:159], v[132:135], v[128:131], v[144:159]
	v_mfma_f32_32x32x16_f16 v[144:159], v[124:127], v[120:123], v[144:159]
	v_mfma_f32_32x32x16_f16 v[144:159], v[116:119], v[112:115], v[144:159]
	s_nop 15
	s_nop 3
	v_max3_f32 v165, v144, v145, v146
	v_max3_f32 v165, v165, v147, v148
	v_max3_f32 v165, v165, v149, v150
	v_max3_f32 v165, v165, v151, v152
	v_max3_f32 v165, v165, v153, v154
	v_max3_f32 v165, v165, v155, v156
	v_max3_f32 v165, v165, v157, v158
	v_max_f32_e32 v165, v165, v159
	v_max_f32_e32 v164, v164, v165
	v_mov_b32_e32 v165, v164
	s_nop 1
	v_permlane32_swap_b32_e32 v164, v165
	v_max_f32_e32 v164, v165, v164
	s_mov_b32 s37, 0x41000000
	v_cmp_lt_f32_e32 vcc, s37, v164
	v_max_f32_e32 v164, 0, v164
	s_nop 4
	s_cbranch_vccnz .Lmy_rare_4_rs
	v_mov_b32_e32 v164, 0
	s_branch .Lmy_rare_4_nr
.Lmy_rare_4_rs:
	v_add_f32_e32 v183, v183, v164
	v_exp_f32_e64 v165, -v164
	s_nop 0
	v_mul_f32_e32 v176, v176, v165
	s_and_saveexec_b64 s[40:41], s[0:1]
	ds_write_b32 v186, v165 offset:57344
	s_or_b64 exec, exec, s[40:41]
	v_add_u32_e32 v166, s11, v182
	s_waitcnt lgkmcnt(0)
	ds_read_b128 v[140:143], v166 offset:57344
	ds_read_b128 v[132:135], v166 offset:57376
	ds_read_b128 v[124:127], v166 offset:57408
	ds_read_b128 v[116:119], v166 offset:57440
	s_waitcnt lgkmcnt(0)
	v_pk_mul_f32 v[16:17], v[16:17], v[140:141]
	v_pk_mul_f32 v[32:33], v[32:33], v[140:141]
	v_pk_mul_f32 v[18:19], v[18:19], v[142:143]
	v_pk_mul_f32 v[34:35], v[34:35], v[142:143]
	v_pk_mul_f32 v[20:21], v[20:21], v[132:133]
	v_pk_mul_f32 v[36:37], v[36:37], v[132:133]
	v_pk_mul_f32 v[22:23], v[22:23], v[134:135]
	v_pk_mul_f32 v[38:39], v[38:39], v[134:135]
	v_pk_mul_f32 v[24:25], v[24:25], v[124:125]
	v_pk_mul_f32 v[40:41], v[40:41], v[124:125]
	v_pk_mul_f32 v[26:27], v[26:27], v[126:127]
	v_pk_mul_f32 v[42:43], v[42:43], v[126:127]
	v_pk_mul_f32 v[28:29], v[28:29], v[116:117]
	v_pk_mul_f32 v[44:45], v[44:45], v[116:117]
	v_pk_mul_f32 v[30:31], v[30:31], v[118:119]
	v_pk_mul_f32 v[46:47], v[46:47], v[118:119]

	.amdhsa_kernel _Z11attn_kernelPKDF16_S0_PDF16_
		.amdhsa_group_segment_fixed_size 0
		.amdhsa_private_segment_fixed_size 0
		.amdhsa_kernarg_size 24
		.amdhsa_user_sgpr_count 2
		.amdhsa_user_sgpr_dispatch_ptr 0
		.amdhsa_user_sgpr_queue_ptr 0
		.amdhsa_user_sgpr_kernarg_segment_ptr 1
		.amdhsa_user_sgpr_dispatch_id 0
		.amdhsa_user_sgpr_kernarg_preload_length 0
		.amdhsa_user_sgpr_kernarg_preload_offset 0
		.amdhsa_user_sgpr_private_segment_size 0
		.amdhsa_uses_dynamic_stack 0
		.amdhsa_enable_private_segment 0
		.amdhsa_system_sgpr_workgroup_id_x 1
		.amdhsa_system_sgpr_workgroup_id_y 0
		.amdhsa_system_sgpr_workgroup_id_z 0
		.amdhsa_system_sgpr_workgroup_info 0
		.amdhsa_system_vgpr_workitem_id 0
		.amdhsa_next_free_vgpr 192
		.amdhsa_next_free_sgpr 50
		.amdhsa_accum_offset 192
		.amdhsa_reserve_vcc 1
		.amdhsa_float_round_mode_32 0
		.amdhsa_float_round_mode_16_64 0
		.amdhsa_float_denorm_mode_32 3
		.amdhsa_float_denorm_mode_16_64 3
		.amdhsa_dx10_clamp 1
		.amdhsa_ieee_mode 1
		.amdhsa_fp16_overflow 0
		.amdhsa_tg_split 0
		.amdhsa_exception_fp_ieee_invalid_op 0
		.amdhsa_exception_fp_denorm_src 0
		.amdhsa_exception_fp_ieee_div_zero 0
		.amdhsa_exception_fp_ieee_overflow 0
		.amdhsa_exception_fp_ieee_underflow 0
		.amdhsa_exception_fp_ieee_inexact 0
		.amdhsa_exception_int_div_zero 0
	.end_amdhsa_kernel

amdhsa.kernels:
  - .agpr_count:     0
    .args:
      - .actual_access:  read_only
        .address_space:  global
        .offset:         0
        .size:           8
        .value_kind:     global_buffer
      - .actual_access:  read_only
        .address_space:  global
        .offset:         8
        .size:           8
        .value_kind:     global_buffer
      - .actual_access:  read_only
        .address_space:  global
        .offset:         16
        .size:           8
        .value_kind:     global_buffer
      - .actual_access:  read_only
        .address_space:  global
        .offset:         24
        .size:           8
        .value_kind:     global_buffer
      - .actual_access:  read_only
        .address_space:  global
        .offset:         32
        .size:           8
        .value_kind:     global_buffer
      - .actual_access:  write_only
        .address_space:  global
        .offset:         40
        .size:           8
        .value_kind:     global_buffer
      - .actual_access:  write_only
        .address_space:  global
        .offset:         48
        .size:           8
        .value_kind:     global_buffer
      - .actual_access:  write_only
        .address_space:  global
        .offset:         56
        .size:           8
        .value_kind:     global_buffer
      - .actual_access:  write_only
        .address_space:  global
        .offset:         64
        .size:           8
        .value_kind:     global_buffer
    .group_segment_fixed_size: 0
    .kernarg_segment_align: 8
    .kernarg_segment_size: 72
    .language:       OpenCL C
    .language_version:
      - 2
      - 0
    .max_flat_workgroup_size: 256
    .name:           _Z11prep_kernelPKfS0_S0_S0_S0_PDF16_S1_S1_S1_
    .private_segment_fixed_size: 0
    .sgpr_count:     21
    .sgpr_spill_count: 0
    .symbol:         _Z11prep_kernelPKfS0_S0_S0_S0_PDF16_S1_S1_S1_.kd
    .uniform_work_group_size: 1
    .uses_dynamic_stack: false
    .vgpr_count:     18
    .vgpr_spill_count: 0
    .wavefront_size: 64
  - .agpr_count:     0
    .args:
      - .actual_access:  read_only
        .address_space:  global
        .offset:         0
        .size:           8
        .value_kind:     global_buffer
      - .actual_access:  read_only
        .address_space:  global
        .offset:         8
        .size:           8
        .value_kind:     global_buffer
      - .actual_access:  read_only
        .address_space:  global
        .offset:         16
        .size:           8
        .value_kind:     global_buffer
      - .actual_access:  read_only
        .address_space:  global
        .offset:         24
        .size:           8
        .value_kind:     global_buffer
      - .actual_access:  read_only
        .address_space:  global
        .offset:         32
        .size:           8
        .value_kind:     global_buffer
      - .actual_access:  write_only
        .address_space:  global
        .offset:         40
        .size:           8
        .value_kind:     global_buffer
      - .actual_access:  write_only
        .address_space:  global
        .offset:         48
        .size:           8
        .value_kind:     global_buffer
    .group_segment_fixed_size: 0
    .kernarg_segment_align: 8
    .kernarg_segment_size: 56
    .language:       OpenCL C
    .language_version:
      - 2
      - 0
    .max_flat_workgroup_size: 512
    .name:           _Z11proj_kernelPKfS0_PKDF16_S0_S0_PDF16_S3_
    .private_segment_fixed_size: 0
    .sgpr_count:     21
    .sgpr_spill_count: 0
    .symbol:         _Z11proj_kernelPKfS0_PKDF16_S0_S0_PDF16_S3_.kd
    .uniform_work_group_size: 1
    .uses_dynamic_stack: false
    .vgpr_count:     170
    .vgpr_spill_count: 0
    .wavefront_size: 64
  - .agpr_count:     0
    .args:
      - .address_space:  global
        .offset:         0
        .size:           8
        .value_kind:     global_buffer
      - .address_space:  global
        .offset:         8
        .size:           8
        .value_kind:     global_buffer
      - .actual_access:  write_only
        .address_space:  global
        .offset:         16
        .size:           8
        .value_kind:     global_buffer
    .group_segment_fixed_size: 0
    .kernarg_segment_align: 8
    .kernarg_segment_size: 24
    .language:       OpenCL C
    .language_version:
      - 2
      - 0
    .max_flat_workgroup_size: 512
    .name:           _Z11attn_kernelPKDF16_S0_PDF16_
    .private_segment_fixed_size: 0
    .sgpr_count:     56
    .sgpr_spill_count: 0
    .symbol:         _Z11attn_kernelPKDF16_S0_PDF16_.kd
    .uniform_work_group_size: 1
    .uses_dynamic_stack: false
    .vgpr_count:     192
    .vgpr_spill_count: 0
    .wavefront_size: 64
  - .agpr_count:     0
    .args:
      - .actual_access:  read_only
        .address_space:  global
        .offset:         0
        .size:           8
        .value_kind:     global_buffer
      - .actual_access:  read_only
        .address_space:  global
        .offset:         8
        .size:           8
        .value_kind:     global_buffer
      - .actual_access:  read_only
        .address_space:  global
        .offset:         16
        .size:           8
        .value_kind:     global_buffer
      - .actual_access:  read_only
        .address_space:  global
        .offset:         24
        .size:           8
        .value_kind:     global_buffer
      - .actual_access:  read_only
        .address_space:  global
        .offset:         32
        .size:           8
        .value_kind:     global_buffer
      - .address_space:  global
        .offset:         40
        .size:           8
        .value_kind:     global_buffer
      - .actual_access:  read_only
        .address_space:  global
        .offset:         48
        .size:           8
        .value_kind:     global_buffer
      - .actual_access:  read_only
        .address_space:  global
        .offset:         56
        .size:           8
        .value_kind:     global_buffer
      - .actual_access:  read_only
        .address_space:  global
        .offset:         64
        .size:           8
        .value_kind:     global_buffer
      - .address_space:  global
        .offset:         72
        .size:           8
        .value_kind:     global_buffer
      - .actual_access:  read_only
        .address_space:  global
        .offset:         80
        .size:           8
        .value_kind:     global_buffer
      - .actual_access:  write_only
        .address_space:  global
        .offset:         88
        .size:           8
        .value_kind:     global_buffer
    .group_segment_fixed_size: 0
    .kernarg_segment_align: 8
    .kernarg_segment_size: 96
    .language:       OpenCL C
    .language_version:
      - 2
      - 0
    .max_flat_workgroup_size: 512
    .name:           _Z10ffn_kernelPKfS0_PKDF16_S2_S0_S2_S0_S0_S0_S2_S0_Pf
    .private_segment_fixed_size: 0
    .sgpr_count:     24
    .sgpr_spill_count: 0
    .symbol:         _Z10ffn_kernelPKfS0_PKDF16_S2_S0_S2_S0_S0_S0_S2_S0_Pf.kd
    .uniform_work_group_size: 1
    .uses_dynamic_stack: false
    .vgpr_count:     230
    .vgpr_spill_count: 0
    .wavefront_size: 64
